# v5: SwiGLU int8 up-GEMM epilogues regenerated with packed f32 math, 4 interleaved chains
# speedup vs baseline: 1.0112x; 1.0046x over previous
; __device__ __forceinline__ float sigmoidf_fast(float x) { return fast_rcp(1.0f + fast_exp2(-x * LOG2E)); }
; #define ROW_FENCE() asm volatile("" ::: "memory")
;     __device__ __forceinline__ void operator()(const pg8::i32x4 (&acc)[2][2][4][2], const pg8::Unit& u, int wr, int wc, int fr, int fq) const {
;         const bool ext = u.pm * 256 >= xrow0; const int roff = ext ? xrow0 : row_off;
;         unsigned char* H = ws + (moe ? (ext ? AR_HREM : AR_HMOE) : AR_HFF)  ; const float* rs = (const float*)(ws + (moe ? WS_SLOTR : WS_RSQ));
;         const float* cp = (const float*)(ws + CTL_AMAX) + (moe ? (size_t)(1 + u.sub) * 2 * DFF : 0) + u.pn * 256 + wc * 32 + 8 * fq;
;         float rsv[2][4];
; #pragma unroll
;         for (int ai = 0; ai < 2; ++ai)
; #pragma unroll
;             for (int m = 0; m < 4; ++m) rsv[ai][m] = rs[u.pm * 256 + ai * 128 + wr * 64 + m * 16 + fr];
;         f32x4 c1[2], c3[2];
; #pragma unroll
;         for (int n = 0; n < 2; ++n) { c1[n] = *(const f32x4*)(cp + 4 * n) * (1.0f / 127.0f); c3[n] = *(const f32x4*)(cp + 128 + 4 * n) * (1.0f / 127.0f); }
; #pragma unroll
;         for (int ai = 0; ai < 2; ++ai)
; #pragma unroll
;             for (int m = 0; m < 4; ++m) {
;                 const int row = u.pm * 256 + ai * 128 + wr * 64 + m * 16 + fr; const float r = rsv[ai][m];
;                 f32x4 h[2];
; #pragma unroll
;                 for (int n = 0; n < 2; ++n)
; #pragma unroll
;                     for (int j = 0; j < 4; ++j) { const float a1 = (float)acc[ai][0][m][n][j] * (r * c1[n][j]), a3 = (float)acc[ai][1][m][n][j] * (r * c3[n][j]); h[n][j] = a1 * sigmoidf_fast(a1) * a3; }
;                 u32x2 w;
; #pragma unroll
;                 for (int n = 0; n < 2; ++n) { int pk = __builtin_amdgcn_cvt_pk_fp8_f32(__builtin_amdgcn_fmed3f(h[n][0], -448.f, 448.f), __builtin_amdgcn_fmed3f(h[n][1], -448.f, 448.f), 0, false);
;                     pk = __builtin_amdgcn_cvt_pk_fp8_f32(__builtin_amdgcn_fmed3f(h[n][2], -448.f, 448.f), __builtin_amdgcn_fmed3f(h[n][3], -448.f, 448.f), pk, true); w[n] = (unsigned)pk; }
;                 if (!dry) *(u32x2*)(H + (size_t)(row - roff) * DFF + u.pn * 128 + wc * 32 + 8 * fq) = w;
;                 ROW_FENCE();
.LBB0_1543:
	v_mbcnt_lo_u32_b32 v138, -1, 0
	v_mbcnt_hi_u32_b32 v138, -1, v138
	s_lshl_b32 s11, s20, 8
	s_mov_b32 s19, 0x1c500000
	s_cmp_lt_i32 s11, s71
	s_cselect_b32 s19, s19, 0x23500000
	s_cselect_b32 s13, s74, s71
	s_add_u32 s20, s34, s19
	s_addc_u32 s21, s35, 0
	s_sub_i32 s11, s11, s13
	s_lshl_b32 s24, s18, 7
	s_add_i32 s24, s24, s6
	v_lshrrev_b32_e32 v139, 1, v138
	v_and_or_b32 v140, v138, 15, s39
	v_and_b32_e32 v139, 24, v139
	v_add_u32_e32 v140, s11, v140
	s_mov_b32 s22, 0x3c010204
	v_mul_u32_u24_e32 v140, 0xe00, v140
	s_mov_b32 s18, 1.0
	v_add3_u32 v140, v140, v139, s24
	s_waitcnt vmcnt(8)
	v_pk_mul_f32 v[206:207], v[206:207], s[22:23] op_sel_hi:[1,0]
	v_pk_mul_f32 v[208:209], v[208:209], s[22:23] op_sel_hi:[1,0]
	v_pk_mul_f32 v[210:211], v[210:211], s[22:23] op_sel_hi:[1,0]
	v_pk_mul_f32 v[212:213], v[212:213], s[22:23] op_sel_hi:[1,0]
	v_pk_mul_f32 v[214:215], v[214:215], s[22:23] op_sel_hi:[1,0]
	v_pk_mul_f32 v[216:217], v[216:217], s[22:23] op_sel_hi:[1,0]
	v_pk_mul_f32 v[218:219], v[218:219], s[22:23] op_sel_hi:[1,0]
	v_pk_mul_f32 v[220:221], v[220:221], s[22:23] op_sel_hi:[1,0]
	v_mul_f32_e32 v237, v229, v229
	v_mul_f32_e32 v236, 0xbfb8aa3b, v229
	v_mul_f32_e32 v235, v228, v228
	v_mul_f32_e32 v234, 0xbfb8aa3b, v228
	v_mul_f32_e32 v233, v227, v227
	v_mul_f32_e32 v232, 0xbfb8aa3b, v227
	v_mul_f32_e32 v231, v226, v226
	v_mul_f32_e32 v230, 0xbfb8aa3b, v226
	v_mul_f32_e32 v229, v225, v225
	v_mul_f32_e32 v228, 0xbfb8aa3b, v225
	v_mul_f32_e32 v227, v224, v224
	v_mul_f32_e32 v226, 0xbfb8aa3b, v224
	v_mul_f32_e32 v225, v223, v223
	v_mul_f32_e32 v224, 0xbfb8aa3b, v223
	v_mul_f32_e32 v223, v222, v222
	v_mul_f32_e32 v222, 0xbfb8aa3b, v222
	v_cvt_f32_i32_e32 v126, v126
	v_cvt_f32_i32_e32 v127, v127
	v_cvt_f32_i32_e32 v128, v128
	v_cvt_f32_i32_e32 v129, v129
	v_cvt_f32_i32_e32 v118, v118
	v_cvt_f32_i32_e32 v119, v119
	v_cvt_f32_i32_e32 v120, v120
	v_cvt_f32_i32_e32 v121, v121
	v_cvt_f32_i32_e32 v122, v122
	v_cvt_f32_i32_e32 v123, v123
	v_cvt_f32_i32_e32 v124, v124
	v_cvt_f32_i32_e32 v125, v125
	v_cvt_f32_i32_e32 v114, v114
	v_cvt_f32_i32_e32 v115, v115
	v_cvt_f32_i32_e32 v116, v116
	v_cvt_f32_i32_e32 v117, v117
	v_pk_mul_f32 v[126:127], v[126:127], v[206:207]
	v_pk_mul_f32 v[128:129], v[128:129], v[208:209]
	v_pk_mul_f32 v[118:119], v[118:119], v[210:211]
	v_pk_mul_f32 v[120:121], v[120:121], v[212:213]
	v_pk_mul_f32 v[166:167], v[126:127], v[222:223] op_sel_hi:[1,0]
	v_pk_mul_f32 v[168:169], v[128:129], v[222:223] op_sel_hi:[1,0]
	v_pk_mul_f32 v[170:171], v[118:119], v[222:223] op_sel_hi:[1,0]
	v_pk_mul_f32 v[172:173], v[120:121], v[222:223] op_sel_hi:[1,0]
	v_pk_mul_f32 v[122:123], v[122:123], v[214:215]
	v_pk_mul_f32 v[124:125], v[124:125], v[216:217]
	v_pk_mul_f32 v[114:115], v[114:115], v[218:219]
	v_pk_mul_f32 v[116:117], v[116:117], v[220:221]
	v_exp_f32_e32 v166, v166
	v_exp_f32_e32 v167, v167
	v_exp_f32_e32 v168, v168
	v_exp_f32_e32 v169, v169
	v_exp_f32_e32 v170, v170
	v_exp_f32_e32 v171, v171
	v_exp_f32_e32 v172, v172
	v_exp_f32_e32 v173, v173
	v_pk_mul_f32 v[126:127], v[126:127], v[122:123]
	v_pk_mul_f32 v[128:129], v[128:129], v[124:125]
	v_pk_mul_f32 v[118:119], v[118:119], v[114:115]
	v_pk_mul_f32 v[120:121], v[120:121], v[116:117]
	v_pk_add_f32 v[166:167], v[166:167], s[18:19] op_sel_hi:[1,0]
	v_pk_add_f32 v[168:169], v[168:169], s[18:19] op_sel_hi:[1,0]
	v_pk_add_f32 v[170:171], v[170:171], s[18:19] op_sel_hi:[1,0]
	v_pk_add_f32 v[172:173], v[172:173], s[18:19] op_sel_hi:[1,0]
	v_pk_mul_f32 v[126:127], v[126:127], v[222:223] op_sel:[0,1] op_sel_hi:[1,1]
	v_pk_mul_f32 v[128:129], v[128:129], v[222:223] op_sel:[0,1] op_sel_hi:[1,1]
	v_pk_mul_f32 v[118:119], v[118:119], v[222:223] op_sel:[0,1] op_sel_hi:[1,1]
	v_pk_mul_f32 v[120:121], v[120:121], v[222:223] op_sel:[0,1] op_sel_hi:[1,1]
	v_rcp_f32_e32 v166, v166
	v_rcp_f32_e32 v167, v167
	v_rcp_f32_e32 v168, v168
	v_rcp_f32_e32 v169, v169
	v_rcp_f32_e32 v170, v170
	v_rcp_f32_e32 v171, v171
	v_rcp_f32_e32 v172, v172
	v_rcp_f32_e32 v173, v173
	v_mov_b32_e32 v141, v140
	v_pk_mul_f32 v[126:127], v[126:127], v[166:167]
	v_pk_mul_f32 v[128:129], v[128:129], v[168:169]
	v_pk_mul_f32 v[118:119], v[118:119], v[170:171]
	v_pk_mul_f32 v[120:121], v[120:121], v[172:173]
	v_med3_f32 v126, v126, s70, v164
	v_med3_f32 v127, v127, s70, v164
	v_med3_f32 v128, v128, s70, v164
	v_med3_f32 v129, v129, s70, v164
	v_med3_f32 v118, v118, s70, v164
	v_med3_f32 v119, v119, s70, v164
	v_med3_f32 v120, v120, s70, v164
	v_med3_f32 v121, v121, s70, v164
	v_cvt_pk_fp8_f32 v160, v126, v127
	v_cvt_pk_fp8_f32 v161, v118, v119
	v_cvt_pk_fp8_f32 v160, v128, v129 op_sel:[0,0,1]
	v_cvt_pk_fp8_f32 v161, v120, v121 op_sel:[0,0,1]
	s_nop 1
	global_store_dwordx2 v141, v[160:161], s[20:21]
	v_cvt_f32_i32_e32 v108, v108
	v_cvt_f32_i32_e32 v109, v109
	v_cvt_f32_i32_e32 v110, v110
	v_cvt_f32_i32_e32 v111, v111
	v_cvt_f32_i32_e32 v100, v100
	v_cvt_f32_i32_e32 v101, v101
	v_cvt_f32_i32_e32 v102, v102
	v_cvt_f32_i32_e32 v103, v103
	v_cvt_f32_i32_e32 v104, v104
	v_cvt_f32_i32_e32 v105, v105
	v_cvt_f32_i32_e32 v106, v106
	v_cvt_f32_i32_e32 v107, v107
	v_cvt_f32_i32_e32 v96, v96
	v_cvt_f32_i32_e32 v97, v97
	v_cvt_f32_i32_e32 v98, v98
	v_cvt_f32_i32_e32 v99, v99
	v_pk_mul_f32 v[108:109], v[108:109], v[206:207]
	v_pk_mul_f32 v[110:111], v[110:111], v[208:209]
	v_pk_mul_f32 v[100:101], v[100:101], v[210:211]
	v_pk_mul_f32 v[102:103], v[102:103], v[212:213]
	v_pk_mul_f32 v[166:167], v[108:109], v[224:225] op_sel_hi:[1,0]
	v_pk_mul_f32 v[168:169], v[110:111], v[224:225] op_sel_hi:[1,0]
	v_pk_mul_f32 v[170:171], v[100:101], v[224:225] op_sel_hi:[1,0]
	v_pk_mul_f32 v[172:173], v[102:103], v[224:225] op_sel_hi:[1,0]
; __device__ __forceinline__ float sigmoidf_fast(float x) { return fast_rcp(1.0f + fast_exp2(-x * LOG2E)); }
; #define ROW_FENCE() asm volatile("" ::: "memory")
;     __device__ __forceinline__ void operator()(const pg8::i32x4 (&acc)[2][2][4][2], const pg8::Unit& u, int wr, int wc, int fr, int fq) const {
;     ...
;         for (int ai = 0; ai < 2; ++ai)
; #pragma unroll
;             for (int m = 0; m < 4; ++m) {
;                 const int row = u.pm * 256 + ai * 128 + wr * 64 + m * 16 + fr; const float r = rsv[ai][m];
;                 f32x4 h[2];
; #pragma unroll
;                 for (int n = 0; n < 2; ++n)
; #pragma unroll
;                     for (int j = 0; j < 4; ++j) { const float a1 = (float)acc[ai][0][m][n][j] * (r * c1[n][j]), a3 = (float)acc[ai][1][m][n][j] * (r * c3[n][j]); h[n][j] = a1 * sigmoidf_fast(a1) * a3; }
;                 u32x2 w;
; #pragma unroll
;                 for (int n = 0; n < 2; ++n) { int pk = __builtin_amdgcn_cvt_pk_fp8_f32(__builtin_amdgcn_fmed3f(h[n][0], -448.f, 448.f), __builtin_amdgcn_fmed3f(h[n][1], -448.f, 448.f), 0, false);
;                     pk = __builtin_amdgcn_cvt_pk_fp8_f32(__builtin_amdgcn_fmed3f(h[n][2], -448.f, 448.f), __builtin_amdgcn_fmed3f(h[n][3], -448.f, 448.f), pk, true); w[n] = (unsigned)pk; }
;                 if (!dry) *(u32x2*)(H + (size_t)(row - roff) * DFF + u.pn * 128 + wc * 32 + 8 * fq) = w;
;                 ROW_FENCE();
	v_pk_mul_f32 v[104:105], v[104:105], v[214:215]
	v_pk_mul_f32 v[106:107], v[106:107], v[216:217]
	v_pk_mul_f32 v[96:97], v[96:97], v[218:219]
	v_pk_mul_f32 v[98:99], v[98:99], v[220:221]
	v_exp_f32_e32 v166, v166
	v_exp_f32_e32 v167, v167
	v_exp_f32_e32 v168, v168
	v_exp_f32_e32 v169, v169
	v_exp_f32_e32 v170, v170
	v_exp_f32_e32 v171, v171
	v_exp_f32_e32 v172, v172
	v_exp_f32_e32 v173, v173
	v_pk_mul_f32 v[108:109], v[108:109], v[104:105]
	v_pk_mul_f32 v[110:111], v[110:111], v[106:107]
	v_pk_mul_f32 v[100:101], v[100:101], v[96:97]
	v_pk_mul_f32 v[102:103], v[102:103], v[98:99]
	v_pk_add_f32 v[166:167], v[166:167], s[18:19] op_sel_hi:[1,0]
	v_pk_add_f32 v[168:169], v[168:169], s[18:19] op_sel_hi:[1,0]
	v_pk_add_f32 v[170:171], v[170:171], s[18:19] op_sel_hi:[1,0]
	v_pk_add_f32 v[172:173], v[172:173], s[18:19] op_sel_hi:[1,0]
	v_pk_mul_f32 v[108:109], v[108:109], v[224:225] op_sel:[0,1] op_sel_hi:[1,1]
	v_pk_mul_f32 v[110:111], v[110:111], v[224:225] op_sel:[0,1] op_sel_hi:[1,1]
	v_pk_mul_f32 v[100:101], v[100:101], v[224:225] op_sel:[0,1] op_sel_hi:[1,1]
	v_pk_mul_f32 v[102:103], v[102:103], v[224:225] op_sel:[0,1] op_sel_hi:[1,1]
	v_rcp_f32_e32 v166, v166
	v_rcp_f32_e32 v167, v167
	v_rcp_f32_e32 v168, v168
	v_rcp_f32_e32 v169, v169
	v_rcp_f32_e32 v170, v170
	v_rcp_f32_e32 v171, v171
	v_rcp_f32_e32 v172, v172
	v_rcp_f32_e32 v173, v173
	v_add_u32_e32 v141, 0xe000, v140
	v_pk_mul_f32 v[108:109], v[108:109], v[166:167]
	v_pk_mul_f32 v[110:111], v[110:111], v[168:169]
	v_pk_mul_f32 v[100:101], v[100:101], v[170:171]
	v_pk_mul_f32 v[102:103], v[102:103], v[172:173]
	v_med3_f32 v108, v108, s70, v164
	v_med3_f32 v109, v109, s70, v164
	v_med3_f32 v110, v110, s70, v164
	v_med3_f32 v111, v111, s70, v164
	v_med3_f32 v100, v100, s70, v164
	v_med3_f32 v101, v101, s70, v164
	v_med3_f32 v102, v102, s70, v164
	v_med3_f32 v103, v103, s70, v164
	v_cvt_pk_fp8_f32 v162, v108, v109
	v_cvt_pk_fp8_f32 v163, v100, v101
	v_cvt_pk_fp8_f32 v162, v110, v111 op_sel:[0,0,1]
	v_cvt_pk_fp8_f32 v163, v102, v103 op_sel:[0,0,1]
	s_nop 1
	global_store_dwordx2 v141, v[162:163], s[20:21]
	v_cvt_f32_i32_e32 v92, v92
	v_cvt_f32_i32_e32 v93, v93
	v_cvt_f32_i32_e32 v94, v94
	v_cvt_f32_i32_e32 v95, v95
	v_cvt_f32_i32_e32 v84, v84
	v_cvt_f32_i32_e32 v85, v85
	v_cvt_f32_i32_e32 v86, v86
	v_cvt_f32_i32_e32 v87, v87
	v_cvt_f32_i32_e32 v88, v88
	v_cvt_f32_i32_e32 v89, v89
	v_cvt_f32_i32_e32 v90, v90
	v_cvt_f32_i32_e32 v91, v91
	v_cvt_f32_i32_e32 v80, v80
	v_cvt_f32_i32_e32 v81, v81
	v_cvt_f32_i32_e32 v82, v82
	v_cvt_f32_i32_e32 v83, v83
	v_pk_mul_f32 v[92:93], v[92:93], v[206:207]
	v_pk_mul_f32 v[94:95], v[94:95], v[208:209]
	v_pk_mul_f32 v[84:85], v[84:85], v[210:211]
	v_pk_mul_f32 v[86:87], v[86:87], v[212:213]
	v_pk_mul_f32 v[166:167], v[92:93], v[226:227] op_sel_hi:[1,0]
	v_pk_mul_f32 v[168:169], v[94:95], v[226:227] op_sel_hi:[1,0]
	v_pk_mul_f32 v[170:171], v[84:85], v[226:227] op_sel_hi:[1,0]
	v_pk_mul_f32 v[172:173], v[86:87], v[226:227] op_sel_hi:[1,0]
	v_pk_mul_f32 v[88:89], v[88:89], v[214:215]
	v_pk_mul_f32 v[90:91], v[90:91], v[216:217]
	v_pk_mul_f32 v[80:81], v[80:81], v[218:219]
	v_pk_mul_f32 v[82:83], v[82:83], v[220:221]
	v_exp_f32_e32 v166, v166
	v_exp_f32_e32 v167, v167
	v_exp_f32_e32 v168, v168
	v_exp_f32_e32 v169, v169
	v_exp_f32_e32 v170, v170
	v_exp_f32_e32 v171, v171
	v_exp_f32_e32 v172, v172
	v_exp_f32_e32 v173, v173
	v_pk_mul_f32 v[92:93], v[92:93], v[88:89]
	v_pk_mul_f32 v[94:95], v[94:95], v[90:91]
	v_pk_mul_f32 v[84:85], v[84:85], v[80:81]
	v_pk_mul_f32 v[86:87], v[86:87], v[82:83]
	v_pk_add_f32 v[166:167], v[166:167], s[18:19] op_sel_hi:[1,0]
	v_pk_add_f32 v[168:169], v[168:169], s[18:19] op_sel_hi:[1,0]
	v_pk_add_f32 v[170:171], v[170:171], s[18:19] op_sel_hi:[1,0]
	v_pk_add_f32 v[172:173], v[172:173], s[18:19] op_sel_hi:[1,0]
	v_pk_mul_f32 v[92:93], v[92:93], v[226:227] op_sel:[0,1] op_sel_hi:[1,1]
	v_pk_mul_f32 v[94:95], v[94:95], v[226:227] op_sel:[0,1] op_sel_hi:[1,1]
	v_pk_mul_f32 v[84:85], v[84:85], v[226:227] op_sel:[0,1] op_sel_hi:[1,1]
	v_pk_mul_f32 v[86:87], v[86:87], v[226:227] op_sel:[0,1] op_sel_hi:[1,1]
	v_rcp_f32_e32 v166, v166
	v_rcp_f32_e32 v167, v167
	v_rcp_f32_e32 v168, v168
	v_rcp_f32_e32 v169, v169
	v_rcp_f32_e32 v170, v170
	v_rcp_f32_e32 v171, v171
	v_rcp_f32_e32 v172, v172
	v_rcp_f32_e32 v173, v173
	v_add_u32_e32 v141, 0x1c000, v140
	v_pk_mul_f32 v[92:93], v[92:93], v[166:167]
	v_pk_mul_f32 v[94:95], v[94:95], v[168:169]
	v_pk_mul_f32 v[84:85], v[84:85], v[170:171]
	v_pk_mul_f32 v[86:87], v[86:87], v[172:173]
	v_med3_f32 v92, v92, s70, v164
	v_med3_f32 v93, v93, s70, v164
	v_med3_f32 v94, v94, s70, v164
	v_med3_f32 v95, v95, s70, v164
	v_med3_f32 v84, v84, s70, v164
	v_med3_f32 v85, v85, s70, v164
	v_med3_f32 v86, v86, s70, v164
	v_med3_f32 v87, v87, s70, v164
	v_cvt_pk_fp8_f32 v160, v92, v93
	v_cvt_pk_fp8_f32 v161, v84, v85
	v_cvt_pk_fp8_f32 v160, v94, v95 op_sel:[0,0,1]
	v_cvt_pk_fp8_f32 v161, v86, v87 op_sel:[0,0,1]
	s_nop 1
	global_store_dwordx2 v141, v[160:161], s[20:21]
	v_cvt_f32_i32_e32 v76, v76
	v_cvt_f32_i32_e32 v77, v77
	v_cvt_f32_i32_e32 v78, v78
	v_cvt_f32_i32_e32 v79, v79
	v_cvt_f32_i32_e32 v68, v68
	v_cvt_f32_i32_e32 v69, v69
	v_cvt_f32_i32_e32 v70, v70
	v_cvt_f32_i32_e32 v71, v71
	v_cvt_f32_i32_e32 v72, v72
	v_cvt_f32_i32_e32 v73, v73
	v_cvt_f32_i32_e32 v74, v74
	v_cvt_f32_i32_e32 v75, v75
	v_cvt_f32_i32_e32 v64, v64
	v_cvt_f32_i32_e32 v65, v65
	v_cvt_f32_i32_e32 v66, v66
	v_cvt_f32_i32_e32 v67, v67
	v_pk_mul_f32 v[76:77], v[76:77], v[206:207]
	v_pk_mul_f32 v[78:79], v[78:79], v[208:209]
	v_pk_mul_f32 v[68:69], v[68:69], v[210:211]
	v_pk_mul_f32 v[70:71], v[70:71], v[212:213]
	v_pk_mul_f32 v[166:167], v[76:77], v[228:229] op_sel_hi:[1,0]
; __device__ __forceinline__ float sigmoidf_fast(float x) { return fast_rcp(1.0f + fast_exp2(-x * LOG2E)); }
; #define ROW_FENCE() asm volatile("" ::: "memory")
;     __device__ __forceinline__ void operator()(const pg8::i32x4 (&acc)[2][2][4][2], const pg8::Unit& u, int wr, int wc, int fr, int fq) const {
;     ...
;         for (int ai = 0; ai < 2; ++ai)
; #pragma unroll
;             for (int m = 0; m < 4; ++m) {
;                 const int row = u.pm * 256 + ai * 128 + wr * 64 + m * 16 + fr; const float r = rsv[ai][m];
;                 f32x4 h[2];
; #pragma unroll
;                 for (int n = 0; n < 2; ++n)
; #pragma unroll
;                     for (int j = 0; j < 4; ++j) { const float a1 = (float)acc[ai][0][m][n][j] * (r * c1[n][j]), a3 = (float)acc[ai][1][m][n][j] * (r * c3[n][j]); h[n][j] = a1 * sigmoidf_fast(a1) * a3; }
;                 u32x2 w;
; #pragma unroll
;                 for (int n = 0; n < 2; ++n) { int pk = __builtin_amdgcn_cvt_pk_fp8_f32(__builtin_amdgcn_fmed3f(h[n][0], -448.f, 448.f), __builtin_amdgcn_fmed3f(h[n][1], -448.f, 448.f), 0, false);
;                     pk = __builtin_amdgcn_cvt_pk_fp8_f32(__builtin_amdgcn_fmed3f(h[n][2], -448.f, 448.f), __builtin_amdgcn_fmed3f(h[n][3], -448.f, 448.f), pk, true); w[n] = (unsigned)pk; }
;                 if (!dry) *(u32x2*)(H + (size_t)(row - roff) * DFF + u.pn * 128 + wc * 32 + 8 * fq) = w;
;                 ROW_FENCE();
	v_pk_mul_f32 v[168:169], v[78:79], v[228:229] op_sel_hi:[1,0]
	v_pk_mul_f32 v[170:171], v[68:69], v[228:229] op_sel_hi:[1,0]
	v_pk_mul_f32 v[172:173], v[70:71], v[228:229] op_sel_hi:[1,0]
	v_pk_mul_f32 v[72:73], v[72:73], v[214:215]
	v_pk_mul_f32 v[74:75], v[74:75], v[216:217]
	v_pk_mul_f32 v[64:65], v[64:65], v[218:219]
	v_pk_mul_f32 v[66:67], v[66:67], v[220:221]
	v_exp_f32_e32 v166, v166
	v_exp_f32_e32 v167, v167
	v_exp_f32_e32 v168, v168
	v_exp_f32_e32 v169, v169
	v_exp_f32_e32 v170, v170
	v_exp_f32_e32 v171, v171
	v_exp_f32_e32 v172, v172
	v_exp_f32_e32 v173, v173
	v_pk_mul_f32 v[76:77], v[76:77], v[72:73]
	v_pk_mul_f32 v[78:79], v[78:79], v[74:75]
	v_pk_mul_f32 v[68:69], v[68:69], v[64:65]
	v_pk_mul_f32 v[70:71], v[70:71], v[66:67]
	v_pk_add_f32 v[166:167], v[166:167], s[18:19] op_sel_hi:[1,0]
	v_pk_add_f32 v[168:169], v[168:169], s[18:19] op_sel_hi:[1,0]
	v_pk_add_f32 v[170:171], v[170:171], s[18:19] op_sel_hi:[1,0]
	v_pk_add_f32 v[172:173], v[172:173], s[18:19] op_sel_hi:[1,0]
	v_pk_mul_f32 v[76:77], v[76:77], v[228:229] op_sel:[0,1] op_sel_hi:[1,1]
	v_pk_mul_f32 v[78:79], v[78:79], v[228:229] op_sel:[0,1] op_sel_hi:[1,1]
	v_pk_mul_f32 v[68:69], v[68:69], v[228:229] op_sel:[0,1] op_sel_hi:[1,1]
	v_pk_mul_f32 v[70:71], v[70:71], v[228:229] op_sel:[0,1] op_sel_hi:[1,1]
	v_rcp_f32_e32 v166, v166
	v_rcp_f32_e32 v167, v167
	v_rcp_f32_e32 v168, v168
	v_rcp_f32_e32 v169, v169
	v_rcp_f32_e32 v170, v170
	v_rcp_f32_e32 v171, v171
	v_rcp_f32_e32 v172, v172
	v_rcp_f32_e32 v173, v173
	v_add_u32_e32 v141, 0x2a000, v140
	v_pk_mul_f32 v[76:77], v[76:77], v[166:167]
	v_pk_mul_f32 v[78:79], v[78:79], v[168:169]
	v_pk_mul_f32 v[68:69], v[68:69], v[170:171]
	v_pk_mul_f32 v[70:71], v[70:71], v[172:173]
	v_med3_f32 v76, v76, s70, v164
	v_med3_f32 v77, v77, s70, v164
	v_med3_f32 v78, v78, s70, v164
	v_med3_f32 v79, v79, s70, v164
	v_med3_f32 v68, v68, s70, v164
	v_med3_f32 v69, v69, s70, v164
	v_med3_f32 v70, v70, s70, v164
	v_med3_f32 v71, v71, s70, v164
	v_cvt_pk_fp8_f32 v162, v76, v77
	v_cvt_pk_fp8_f32 v163, v68, v69
	v_cvt_pk_fp8_f32 v162, v78, v79 op_sel:[0,0,1]
	v_cvt_pk_fp8_f32 v163, v70, v71 op_sel:[0,0,1]
	s_nop 1
	global_store_dwordx2 v141, v[162:163], s[20:21]
	v_cvt_f32_i32_e32 v60, v60
	v_cvt_f32_i32_e32 v61, v61
	v_cvt_f32_i32_e32 v62, v62
	v_cvt_f32_i32_e32 v63, v63
	v_cvt_f32_i32_e32 v52, v52
	v_cvt_f32_i32_e32 v53, v53
	v_cvt_f32_i32_e32 v54, v54
	v_cvt_f32_i32_e32 v55, v55
	v_cvt_f32_i32_e32 v56, v56
	v_cvt_f32_i32_e32 v57, v57
	v_cvt_f32_i32_e32 v58, v58
	v_cvt_f32_i32_e32 v59, v59
	v_cvt_f32_i32_e32 v48, v48
	v_cvt_f32_i32_e32 v49, v49
	v_cvt_f32_i32_e32 v50, v50
	v_cvt_f32_i32_e32 v51, v51
	v_pk_mul_f32 v[60:61], v[60:61], v[206:207]
	v_pk_mul_f32 v[62:63], v[62:63], v[208:209]
	v_pk_mul_f32 v[52:53], v[52:53], v[210:211]
	v_pk_mul_f32 v[54:55], v[54:55], v[212:213]
	v_pk_mul_f32 v[166:167], v[60:61], v[230:231] op_sel_hi:[1,0]
	v_pk_mul_f32 v[168:169], v[62:63], v[230:231] op_sel_hi:[1,0]
	v_pk_mul_f32 v[170:171], v[52:53], v[230:231] op_sel_hi:[1,0]
	v_pk_mul_f32 v[172:173], v[54:55], v[230:231] op_sel_hi:[1,0]
	v_pk_mul_f32 v[56:57], v[56:57], v[214:215]
	v_pk_mul_f32 v[58:59], v[58:59], v[216:217]
	v_pk_mul_f32 v[48:49], v[48:49], v[218:219]
	v_pk_mul_f32 v[50:51], v[50:51], v[220:221]
	v_exp_f32_e32 v166, v166
	v_exp_f32_e32 v167, v167
	v_exp_f32_e32 v168, v168
	v_exp_f32_e32 v169, v169
	v_exp_f32_e32 v170, v170
	v_exp_f32_e32 v171, v171
	v_exp_f32_e32 v172, v172
	v_exp_f32_e32 v173, v173
	v_pk_mul_f32 v[60:61], v[60:61], v[56:57]
	v_pk_mul_f32 v[62:63], v[62:63], v[58:59]
	v_pk_mul_f32 v[52:53], v[52:53], v[48:49]
	v_pk_mul_f32 v[54:55], v[54:55], v[50:51]
	v_pk_add_f32 v[166:167], v[166:167], s[18:19] op_sel_hi:[1,0]
	v_pk_add_f32 v[168:169], v[168:169], s[18:19] op_sel_hi:[1,0]
	v_pk_add_f32 v[170:171], v[170:171], s[18:19] op_sel_hi:[1,0]
	v_pk_add_f32 v[172:173], v[172:173], s[18:19] op_sel_hi:[1,0]
	v_pk_mul_f32 v[60:61], v[60:61], v[230:231] op_sel:[0,1] op_sel_hi:[1,1]
	v_pk_mul_f32 v[62:63], v[62:63], v[230:231] op_sel:[0,1] op_sel_hi:[1,1]
	v_pk_mul_f32 v[52:53], v[52:53], v[230:231] op_sel:[0,1] op_sel_hi:[1,1]
	v_pk_mul_f32 v[54:55], v[54:55], v[230:231] op_sel:[0,1] op_sel_hi:[1,1]
	v_rcp_f32_e32 v166, v166
	v_rcp_f32_e32 v167, v167
	v_rcp_f32_e32 v168, v168
	v_rcp_f32_e32 v169, v169
	v_rcp_f32_e32 v170, v170
	v_rcp_f32_e32 v171, v171
	v_rcp_f32_e32 v172, v172
	v_rcp_f32_e32 v173, v173
	v_add_u32_e32 v141, 0x70000, v140
	v_pk_mul_f32 v[60:61], v[60:61], v[166:167]
	v_pk_mul_f32 v[62:63], v[62:63], v[168:169]
	v_pk_mul_f32 v[52:53], v[52:53], v[170:171]
	v_pk_mul_f32 v[54:55], v[54:55], v[172:173]
	v_med3_f32 v60, v60, s70, v164
	v_med3_f32 v61, v61, s70, v164
	v_med3_f32 v62, v62, s70, v164
	v_med3_f32 v63, v63, s70, v164
	v_med3_f32 v52, v52, s70, v164
	v_med3_f32 v53, v53, s70, v164
	v_med3_f32 v54, v54, s70, v164
	v_med3_f32 v55, v55, s70, v164
	v_cvt_pk_fp8_f32 v160, v60, v61
	v_cvt_pk_fp8_f32 v161, v52, v53
	v_cvt_pk_fp8_f32 v160, v62, v63 op_sel:[0,0,1]
	v_cvt_pk_fp8_f32 v161, v54, v55 op_sel:[0,0,1]
	s_nop 1
	global_store_dwordx2 v141, v[160:161], s[20:21]
	v_cvt_f32_i32_e32 v44, v44
	v_cvt_f32_i32_e32 v45, v45
	v_cvt_f32_i32_e32 v46, v46
	v_cvt_f32_i32_e32 v47, v47
	v_cvt_f32_i32_e32 v36, v36
	v_cvt_f32_i32_e32 v37, v37
	v_cvt_f32_i32_e32 v38, v38
	v_cvt_f32_i32_e32 v39, v39
	v_cvt_f32_i32_e32 v40, v40
	v_cvt_f32_i32_e32 v41, v41
	v_cvt_f32_i32_e32 v42, v42
	v_cvt_f32_i32_e32 v43, v43
	v_cvt_f32_i32_e32 v32, v32
	v_cvt_f32_i32_e32 v33, v33
	v_cvt_f32_i32_e32 v34, v34
	v_cvt_f32_i32_e32 v35, v35
	v_pk_mul_f32 v[44:45], v[44:45], v[206:207]
	v_pk_mul_f32 v[46:47], v[46:47], v[208:209]
; __device__ __forceinline__ float sigmoidf_fast(float x) { return fast_rcp(1.0f + fast_exp2(-x * LOG2E)); }
; #define ROW_FENCE() asm volatile("" ::: "memory")
;     __device__ __forceinline__ void operator()(const pg8::i32x4 (&acc)[2][2][4][2], const pg8::Unit& u, int wr, int wc, int fr, int fq) const {
;     ...
;         for (int ai = 0; ai < 2; ++ai)
; #pragma unroll
;             for (int m = 0; m < 4; ++m) {
;                 const int row = u.pm * 256 + ai * 128 + wr * 64 + m * 16 + fr; const float r = rsv[ai][m];
;                 f32x4 h[2];
; #pragma unroll
;                 for (int n = 0; n < 2; ++n)
; #pragma unroll
;                     for (int j = 0; j < 4; ++j) { const float a1 = (float)acc[ai][0][m][n][j] * (r * c1[n][j]), a3 = (float)acc[ai][1][m][n][j] * (r * c3[n][j]); h[n][j] = a1 * sigmoidf_fast(a1) * a3; }
;                 u32x2 w;
; #pragma unroll
;                 for (int n = 0; n < 2; ++n) { int pk = __builtin_amdgcn_cvt_pk_fp8_f32(__builtin_amdgcn_fmed3f(h[n][0], -448.f, 448.f), __builtin_amdgcn_fmed3f(h[n][1], -448.f, 448.f), 0, false);
;                     pk = __builtin_amdgcn_cvt_pk_fp8_f32(__builtin_amdgcn_fmed3f(h[n][2], -448.f, 448.f), __builtin_amdgcn_fmed3f(h[n][3], -448.f, 448.f), pk, true); w[n] = (unsigned)pk; }
;                 if (!dry) *(u32x2*)(H + (size_t)(row - roff) * DFF + u.pn * 128 + wc * 32 + 8 * fq) = w;
;                 ROW_FENCE();
	v_pk_mul_f32 v[36:37], v[36:37], v[210:211]
	v_pk_mul_f32 v[38:39], v[38:39], v[212:213]
	v_pk_mul_f32 v[166:167], v[44:45], v[232:233] op_sel_hi:[1,0]
	v_pk_mul_f32 v[168:169], v[46:47], v[232:233] op_sel_hi:[1,0]
	v_pk_mul_f32 v[170:171], v[36:37], v[232:233] op_sel_hi:[1,0]
	v_pk_mul_f32 v[172:173], v[38:39], v[232:233] op_sel_hi:[1,0]
	v_pk_mul_f32 v[40:41], v[40:41], v[214:215]
	v_pk_mul_f32 v[42:43], v[42:43], v[216:217]
	v_pk_mul_f32 v[32:33], v[32:33], v[218:219]
	v_pk_mul_f32 v[34:35], v[34:35], v[220:221]
	v_exp_f32_e32 v166, v166
	v_exp_f32_e32 v167, v167
	v_exp_f32_e32 v168, v168
	v_exp_f32_e32 v169, v169
	v_exp_f32_e32 v170, v170
	v_exp_f32_e32 v171, v171
	v_exp_f32_e32 v172, v172
	v_exp_f32_e32 v173, v173
	v_pk_mul_f32 v[44:45], v[44:45], v[40:41]
	v_pk_mul_f32 v[46:47], v[46:47], v[42:43]
	v_pk_mul_f32 v[36:37], v[36:37], v[32:33]
	v_pk_mul_f32 v[38:39], v[38:39], v[34:35]
	v_pk_add_f32 v[166:167], v[166:167], s[18:19] op_sel_hi:[1,0]
	v_pk_add_f32 v[168:169], v[168:169], s[18:19] op_sel_hi:[1,0]
	v_pk_add_f32 v[170:171], v[170:171], s[18:19] op_sel_hi:[1,0]
	v_pk_add_f32 v[172:173], v[172:173], s[18:19] op_sel_hi:[1,0]
	v_pk_mul_f32 v[44:45], v[44:45], v[232:233] op_sel:[0,1] op_sel_hi:[1,1]
	v_pk_mul_f32 v[46:47], v[46:47], v[232:233] op_sel:[0,1] op_sel_hi:[1,1]
	v_pk_mul_f32 v[36:37], v[36:37], v[232:233] op_sel:[0,1] op_sel_hi:[1,1]
	v_pk_mul_f32 v[38:39], v[38:39], v[232:233] op_sel:[0,1] op_sel_hi:[1,1]
	v_rcp_f32_e32 v166, v166
	v_rcp_f32_e32 v167, v167
	v_rcp_f32_e32 v168, v168
	v_rcp_f32_e32 v169, v169
	v_rcp_f32_e32 v170, v170
	v_rcp_f32_e32 v171, v171
	v_rcp_f32_e32 v172, v172
	v_rcp_f32_e32 v173, v173
	v_add_u32_e32 v141, 0x7e000, v140
	v_pk_mul_f32 v[44:45], v[44:45], v[166:167]
	v_pk_mul_f32 v[46:47], v[46:47], v[168:169]
	v_pk_mul_f32 v[36:37], v[36:37], v[170:171]
	v_pk_mul_f32 v[38:39], v[38:39], v[172:173]
	v_med3_f32 v44, v44, s70, v164
	v_med3_f32 v45, v45, s70, v164
	v_med3_f32 v46, v46, s70, v164
	v_med3_f32 v47, v47, s70, v164
	v_med3_f32 v36, v36, s70, v164
	v_med3_f32 v37, v37, s70, v164
	v_med3_f32 v38, v38, s70, v164
	v_med3_f32 v39, v39, s70, v164
	v_cvt_pk_fp8_f32 v162, v44, v45
	v_cvt_pk_fp8_f32 v163, v36, v37
	v_cvt_pk_fp8_f32 v162, v46, v47 op_sel:[0,0,1]
	v_cvt_pk_fp8_f32 v163, v38, v39 op_sel:[0,0,1]
	s_nop 1
	global_store_dwordx2 v141, v[162:163], s[20:21]
	v_cvt_f32_i32_e32 v28, v28
	v_cvt_f32_i32_e32 v29, v29
	v_cvt_f32_i32_e32 v30, v30
	v_cvt_f32_i32_e32 v31, v31
	v_cvt_f32_i32_e32 v20, v20
	v_cvt_f32_i32_e32 v21, v21
	v_cvt_f32_i32_e32 v22, v22
	v_cvt_f32_i32_e32 v23, v23
	v_cvt_f32_i32_e32 v24, v24
	v_cvt_f32_i32_e32 v25, v25
	v_cvt_f32_i32_e32 v26, v26
	v_cvt_f32_i32_e32 v27, v27
	v_cvt_f32_i32_e32 v16, v16
	v_cvt_f32_i32_e32 v17, v17
	v_cvt_f32_i32_e32 v18, v18
	v_cvt_f32_i32_e32 v19, v19
	v_pk_mul_f32 v[28:29], v[28:29], v[206:207]
	v_pk_mul_f32 v[30:31], v[30:31], v[208:209]
	v_pk_mul_f32 v[20:21], v[20:21], v[210:211]
	v_pk_mul_f32 v[22:23], v[22:23], v[212:213]
	v_pk_mul_f32 v[166:167], v[28:29], v[234:235] op_sel_hi:[1,0]
	v_pk_mul_f32 v[168:169], v[30:31], v[234:235] op_sel_hi:[1,0]
	v_pk_mul_f32 v[170:171], v[20:21], v[234:235] op_sel_hi:[1,0]
	v_pk_mul_f32 v[172:173], v[22:23], v[234:235] op_sel_hi:[1,0]
	v_pk_mul_f32 v[24:25], v[24:25], v[214:215]
	v_pk_mul_f32 v[26:27], v[26:27], v[216:217]
	v_pk_mul_f32 v[16:17], v[16:17], v[218:219]
	v_pk_mul_f32 v[18:19], v[18:19], v[220:221]
	v_exp_f32_e32 v166, v166
	v_exp_f32_e32 v167, v167
	v_exp_f32_e32 v168, v168
	v_exp_f32_e32 v169, v169
	v_exp_f32_e32 v170, v170
	v_exp_f32_e32 v171, v171
	v_exp_f32_e32 v172, v172
	v_exp_f32_e32 v173, v173
	v_pk_mul_f32 v[28:29], v[28:29], v[24:25]
	v_pk_mul_f32 v[30:31], v[30:31], v[26:27]
	v_pk_mul_f32 v[20:21], v[20:21], v[16:17]
	v_pk_mul_f32 v[22:23], v[22:23], v[18:19]
	v_pk_add_f32 v[166:167], v[166:167], s[18:19] op_sel_hi:[1,0]
	v_pk_add_f32 v[168:169], v[168:169], s[18:19] op_sel_hi:[1,0]
	v_pk_add_f32 v[170:171], v[170:171], s[18:19] op_sel_hi:[1,0]
	v_pk_add_f32 v[172:173], v[172:173], s[18:19] op_sel_hi:[1,0]
	v_pk_mul_f32 v[28:29], v[28:29], v[234:235] op_sel:[0,1] op_sel_hi:[1,1]
; __device__ __forceinline__ float sigmoidf_fast(float x) { return fast_rcp(1.0f + fast_exp2(-x * LOG2E)); }
; #define ROW_FENCE() asm volatile("" ::: "memory")
;     __device__ __forceinline__ void operator()(const pg8::i32x4 (&acc)[2][2][4][2], const pg8::Unit& u, int wr, int wc, int fr, int fq) const {
;     ...
;         for (int ai = 0; ai < 2; ++ai)
; #pragma unroll
;             for (int m = 0; m < 4; ++m) {
;                 const int row = u.pm * 256 + ai * 128 + wr * 64 + m * 16 + fr; const float r = rsv[ai][m];
;                 f32x4 h[2];
; #pragma unroll
;                 for (int n = 0; n < 2; ++n)
; #pragma unroll
;                     for (int j = 0; j < 4; ++j) { const float a1 = (float)acc[ai][0][m][n][j] * (r * c1[n][j]), a3 = (float)acc[ai][1][m][n][j] * (r * c3[n][j]); h[n][j] = a1 * sigmoidf_fast(a1) * a3; }
;                 u32x2 w;
; #pragma unroll
;                 for (int n = 0; n < 2; ++n) { int pk = __builtin_amdgcn_cvt_pk_fp8_f32(__builtin_amdgcn_fmed3f(h[n][0], -448.f, 448.f), __builtin_amdgcn_fmed3f(h[n][1], -448.f, 448.f), 0, false);
;                     pk = __builtin_amdgcn_cvt_pk_fp8_f32(__builtin_amdgcn_fmed3f(h[n][2], -448.f, 448.f), __builtin_amdgcn_fmed3f(h[n][3], -448.f, 448.f), pk, true); w[n] = (unsigned)pk; }
;                 if (!dry) *(u32x2*)(H + (size_t)(row - roff) * DFF + u.pn * 128 + wc * 32 + 8 * fq) = w;
;                 ROW_FENCE();
	v_pk_mul_f32 v[30:31], v[30:31], v[234:235] op_sel:[0,1] op_sel_hi:[1,1]
	v_pk_mul_f32 v[20:21], v[20:21], v[234:235] op_sel:[0,1] op_sel_hi:[1,1]
	v_pk_mul_f32 v[22:23], v[22:23], v[234:235] op_sel:[0,1] op_sel_hi:[1,1]
	v_rcp_f32_e32 v166, v166
	v_rcp_f32_e32 v167, v167
	v_rcp_f32_e32 v168, v168
	v_rcp_f32_e32 v169, v169
	v_rcp_f32_e32 v170, v170
	v_rcp_f32_e32 v171, v171
	v_rcp_f32_e32 v172, v172
	v_rcp_f32_e32 v173, v173
	v_add_u32_e32 v141, 0x8c000, v140
	v_pk_mul_f32 v[28:29], v[28:29], v[166:167]
	v_pk_mul_f32 v[30:31], v[30:31], v[168:169]
	v_pk_mul_f32 v[20:21], v[20:21], v[170:171]
	v_pk_mul_f32 v[22:23], v[22:23], v[172:173]
	v_med3_f32 v28, v28, s70, v164
	v_med3_f32 v29, v29, s70, v164
	v_med3_f32 v30, v30, s70, v164
	v_med3_f32 v31, v31, s70, v164
	v_med3_f32 v20, v20, s70, v164
	v_med3_f32 v21, v21, s70, v164
	v_med3_f32 v22, v22, s70, v164
	v_med3_f32 v23, v23, s70, v164
	v_cvt_pk_fp8_f32 v160, v28, v29
	v_cvt_pk_fp8_f32 v161, v20, v21
	v_cvt_pk_fp8_f32 v160, v30, v31 op_sel:[0,0,1]
	v_cvt_pk_fp8_f32 v161, v22, v23 op_sel:[0,0,1]
	s_nop 1
	global_store_dwordx2 v141, v[160:161], s[20:21]
	v_cvt_f32_i32_e32 v12, v12
	v_cvt_f32_i32_e32 v13, v13
	v_cvt_f32_i32_e32 v14, v14
	v_cvt_f32_i32_e32 v15, v15
	v_cvt_f32_i32_e32 v4, v4
	v_cvt_f32_i32_e32 v5, v5
	v_cvt_f32_i32_e32 v6, v6
	v_cvt_f32_i32_e32 v7, v7
	v_cvt_f32_i32_e32 v8, v8
	v_cvt_f32_i32_e32 v9, v9
	v_cvt_f32_i32_e32 v10, v10
	v_cvt_f32_i32_e32 v11, v11
	v_cvt_f32_i32_e32 v0, v0
	v_cvt_f32_i32_e32 v1, v1
	v_cvt_f32_i32_e32 v2, v2
	v_cvt_f32_i32_e32 v3, v3
	v_pk_mul_f32 v[12:13], v[12:13], v[206:207]
	v_pk_mul_f32 v[14:15], v[14:15], v[208:209]
	v_pk_mul_f32 v[4:5], v[4:5], v[210:211]
	v_pk_mul_f32 v[6:7], v[6:7], v[212:213]
	v_pk_mul_f32 v[166:167], v[12:13], v[236:237] op_sel_hi:[1,0]
	v_pk_mul_f32 v[168:169], v[14:15], v[236:237] op_sel_hi:[1,0]
	v_pk_mul_f32 v[170:171], v[4:5], v[236:237] op_sel_hi:[1,0]
	v_pk_mul_f32 v[172:173], v[6:7], v[236:237] op_sel_hi:[1,0]
	v_pk_mul_f32 v[8:9], v[8:9], v[214:215]
	v_pk_mul_f32 v[10:11], v[10:11], v[216:217]
	v_pk_mul_f32 v[0:1], v[0:1], v[218:219]
	v_pk_mul_f32 v[2:3], v[2:3], v[220:221]
	v_exp_f32_e32 v166, v166
	v_exp_f32_e32 v167, v167
	v_exp_f32_e32 v168, v168
	v_exp_f32_e32 v169, v169
	v_exp_f32_e32 v170, v170
	v_exp_f32_e32 v171, v171
	v_exp_f32_e32 v172, v172
	v_exp_f32_e32 v173, v173
	v_pk_mul_f32 v[12:13], v[12:13], v[8:9]
	v_pk_mul_f32 v[14:15], v[14:15], v[10:11]
	v_pk_mul_f32 v[4:5], v[4:5], v[0:1]
	v_pk_mul_f32 v[6:7], v[6:7], v[2:3]
	v_pk_add_f32 v[166:167], v[166:167], s[18:19] op_sel_hi:[1,0]
	v_pk_add_f32 v[168:169], v[168:169], s[18:19] op_sel_hi:[1,0]
	v_pk_add_f32 v[170:171], v[170:171], s[18:19] op_sel_hi:[1,0]
	v_pk_add_f32 v[172:173], v[172:173], s[18:19] op_sel_hi:[1,0]
	v_pk_mul_f32 v[12:13], v[12:13], v[236:237] op_sel:[0,1] op_sel_hi:[1,1]
	v_pk_mul_f32 v[14:15], v[14:15], v[236:237] op_sel:[0,1] op_sel_hi:[1,1]
	v_pk_mul_f32 v[4:5], v[4:5], v[236:237] op_sel:[0,1] op_sel_hi:[1,1]
	v_pk_mul_f32 v[6:7], v[6:7], v[236:237] op_sel:[0,1] op_sel_hi:[1,1]
	v_rcp_f32_e32 v166, v166
	v_rcp_f32_e32 v167, v167
	v_rcp_f32_e32 v168, v168
	v_rcp_f32_e32 v169, v169
	v_rcp_f32_e32 v170, v170
	v_rcp_f32_e32 v171, v171
	v_rcp_f32_e32 v172, v172
	v_rcp_f32_e32 v173, v173
	v_add_u32_e32 v141, 0x9a000, v140
	v_pk_mul_f32 v[12:13], v[12:13], v[166:167]
	v_pk_mul_f32 v[14:15], v[14:15], v[168:169]
	v_pk_mul_f32 v[4:5], v[4:5], v[170:171]
	v_pk_mul_f32 v[6:7], v[6:7], v[172:173]
	v_med3_f32 v12, v12, s70, v164
	v_med3_f32 v13, v13, s70, v164
	v_med3_f32 v14, v14, s70, v164
	v_med3_f32 v15, v15, s70, v164
	v_med3_f32 v4, v4, s70, v164
	v_med3_f32 v5, v5, s70, v164
	v_med3_f32 v6, v6, s70, v164
	v_med3_f32 v7, v7, s70, v164
	v_cvt_pk_fp8_f32 v162, v12, v13
	v_cvt_pk_fp8_f32 v163, v4, v5
	v_cvt_pk_fp8_f32 v162, v14, v15 op_sel:[0,0,1]
	v_cvt_pk_fp8_f32 v163, v6, v7 op_sel:[0,0,1]
	s_nop 1
	global_store_dwordx2 v141, v[162:163], s[20:21]
	s_andn2_b64 vcc, exec, s[2:3]
	s_mov_b64 s[18:19], -1
	s_cbranch_vccnz .LBB0_1532
	s_andn2_b64 vcc, exec, s[4:5]
	s_cbranch_vccnz .LBB0_1531
	s_barrier
	s_branch .LBB0_1531

; __device__ __forceinline__ float sigmoidf_fast(float x) { return fast_rcp(1.0f + fast_exp2(-x * LOG2E)); }
; #define ROW_FENCE() asm volatile("" ::: "memory")
;     __device__ __forceinline__ void operator()(const pg8::i32x4 (&acc)[2][2][4][2], const pg8::Unit& u, int wr, int wc, int fr, int fq) const {
;         const bool ext = u.pm * 256 >= xrow0; const int roff = ext ? xrow0 : row_off;
;         unsigned char* H = ws + (moe ? (ext ? AR_HREM : AR_HMOE) : AR_HFF)  ; const float* rs = (const float*)(ws + (moe ? WS_SLOTR : WS_RSQ));
;         const float* cp = (const float*)(ws + CTL_AMAX) + (moe ? (size_t)(1 + u.sub) * 2 * DFF : 0) + u.pn * 256 + wc * 32 + 8 * fq;
;         float rsv[2][4];
; #pragma unroll
;         for (int ai = 0; ai < 2; ++ai)
; #pragma unroll
;             for (int m = 0; m < 4; ++m) rsv[ai][m] = rs[u.pm * 256 + ai * 128 + wr * 64 + m * 16 + fr];
;         f32x4 c1[2], c3[2];
; #pragma unroll
;         for (int n = 0; n < 2; ++n) { c1[n] = *(const f32x4*)(cp + 4 * n) * (1.0f / 127.0f); c3[n] = *(const f32x4*)(cp + 128 + 4 * n) * (1.0f / 127.0f); }
; #pragma unroll
;         for (int ai = 0; ai < 2; ++ai)
; #pragma unroll
;             for (int m = 0; m < 4; ++m) {
;                 const int row = u.pm * 256 + ai * 128 + wr * 64 + m * 16 + fr; const float r = rsv[ai][m];
;                 f32x4 h[2];
; #pragma unroll
;                 for (int n = 0; n < 2; ++n)
; #pragma unroll
;                     for (int j = 0; j < 4; ++j) { const float a1 = (float)acc[ai][0][m][n][j] * (r * c1[n][j]), a3 = (float)acc[ai][1][m][n][j] * (r * c3[n][j]); h[n][j] = a1 * sigmoidf_fast(a1) * a3; }
;                 u32x2 w;
; #pragma unroll
;                 for (int n = 0; n < 2; ++n) { int pk = __builtin_amdgcn_cvt_pk_fp8_f32(__builtin_amdgcn_fmed3f(h[n][0], -448.f, 448.f), __builtin_amdgcn_fmed3f(h[n][1], -448.f, 448.f), 0, false);
;                     pk = __builtin_amdgcn_cvt_pk_fp8_f32(__builtin_amdgcn_fmed3f(h[n][2], -448.f, 448.f), __builtin_amdgcn_fmed3f(h[n][3], -448.f, 448.f), pk, true); w[n] = (unsigned)pk; }
;                 if (!dry) *(u32x2*)(H + (size_t)(row - roff) * DFF + u.pn * 128 + wc * 32 + 8 * fq) = w;
;                 ROW_FENCE();
.LBB0_1770:
	v_mbcnt_lo_u32_b32 v138, -1, 0
	v_mbcnt_hi_u32_b32 v138, -1, v138
	s_lshl_b32 s9, s17, 7
	v_lshrrev_b32_e32 v139, 1, v138
	s_add_i32 s9, s9, s92
	v_and_or_b32 v140, v138, 15, s42
	v_and_b32_e32 v139, 24, v139
	v_lshl_add_u32 v140, s16, 8, v140
	s_mov_b32 s18, 0x3c010204
	v_mul_u32_u24_e32 v140, 0xe00, v140
	s_mov_b32 s16, 1.0
	v_add3_u32 v140, v140, v139, s9
	s_waitcnt vmcnt(8)
	v_pk_mul_f32 v[206:207], v[206:207], s[18:19] op_sel_hi:[1,0]
	v_pk_mul_f32 v[208:209], v[208:209], s[18:19] op_sel_hi:[1,0]
	v_pk_mul_f32 v[210:211], v[210:211], s[18:19] op_sel_hi:[1,0]
	v_pk_mul_f32 v[212:213], v[212:213], s[18:19] op_sel_hi:[1,0]
	v_pk_mul_f32 v[214:215], v[214:215], s[18:19] op_sel_hi:[1,0]
	v_pk_mul_f32 v[216:217], v[216:217], s[18:19] op_sel_hi:[1,0]
	v_pk_mul_f32 v[218:219], v[218:219], s[18:19] op_sel_hi:[1,0]
	v_pk_mul_f32 v[220:221], v[220:221], s[18:19] op_sel_hi:[1,0]
	v_mul_f32_e32 v237, v229, v229
	v_mul_f32_e32 v236, 0xbfb8aa3b, v229
	v_mul_f32_e32 v235, v228, v228
	v_mul_f32_e32 v234, 0xbfb8aa3b, v228
	v_mul_f32_e32 v233, v227, v227
	v_mul_f32_e32 v232, 0xbfb8aa3b, v227
	v_mul_f32_e32 v231, v226, v226
	v_mul_f32_e32 v230, 0xbfb8aa3b, v226
	v_mul_f32_e32 v229, v225, v225
	v_mul_f32_e32 v228, 0xbfb8aa3b, v225
	v_mul_f32_e32 v227, v224, v224
	v_mul_f32_e32 v226, 0xbfb8aa3b, v224
	v_mul_f32_e32 v225, v223, v223
	v_mul_f32_e32 v224, 0xbfb8aa3b, v223
	v_mul_f32_e32 v223, v222, v222
	v_mul_f32_e32 v222, 0xbfb8aa3b, v222
	v_cvt_f32_i32_e32 v126, v126
	v_cvt_f32_i32_e32 v127, v127
	v_cvt_f32_i32_e32 v128, v128
	v_cvt_f32_i32_e32 v129, v129
	v_cvt_f32_i32_e32 v118, v118
	v_cvt_f32_i32_e32 v119, v119
	v_cvt_f32_i32_e32 v120, v120
	v_cvt_f32_i32_e32 v121, v121
	v_cvt_f32_i32_e32 v122, v122
	v_cvt_f32_i32_e32 v123, v123
	v_cvt_f32_i32_e32 v124, v124
	v_cvt_f32_i32_e32 v125, v125
	v_cvt_f32_i32_e32 v114, v114
	v_cvt_f32_i32_e32 v115, v115
	v_cvt_f32_i32_e32 v116, v116
	v_cvt_f32_i32_e32 v117, v117
	v_pk_mul_f32 v[126:127], v[126:127], v[206:207]
	v_pk_mul_f32 v[128:129], v[128:129], v[208:209]
	v_pk_mul_f32 v[118:119], v[118:119], v[210:211]
	v_pk_mul_f32 v[120:121], v[120:121], v[212:213]
	v_pk_mul_f32 v[172:173], v[126:127], v[222:223] op_sel_hi:[1,0]
	v_pk_mul_f32 v[174:175], v[128:129], v[222:223] op_sel_hi:[1,0]
	v_pk_mul_f32 v[176:177], v[118:119], v[222:223] op_sel_hi:[1,0]
	v_pk_mul_f32 v[178:179], v[120:121], v[222:223] op_sel_hi:[1,0]
	v_pk_mul_f32 v[122:123], v[122:123], v[214:215]
	v_pk_mul_f32 v[124:125], v[124:125], v[216:217]
	v_pk_mul_f32 v[114:115], v[114:115], v[218:219]
	v_pk_mul_f32 v[116:117], v[116:117], v[220:221]
	v_exp_f32_e32 v172, v172
	v_exp_f32_e32 v173, v173
	v_exp_f32_e32 v174, v174
	v_exp_f32_e32 v175, v175
	v_exp_f32_e32 v176, v176
	v_exp_f32_e32 v177, v177
	v_exp_f32_e32 v178, v178
	v_exp_f32_e32 v179, v179
	v_pk_mul_f32 v[126:127], v[126:127], v[122:123]
	v_pk_mul_f32 v[128:129], v[128:129], v[124:125]
	v_pk_mul_f32 v[118:119], v[118:119], v[114:115]
	v_pk_mul_f32 v[120:121], v[120:121], v[116:117]
	v_pk_add_f32 v[172:173], v[172:173], s[16:17] op_sel_hi:[1,0]
	v_pk_add_f32 v[174:175], v[174:175], s[16:17] op_sel_hi:[1,0]
	v_pk_add_f32 v[176:177], v[176:177], s[16:17] op_sel_hi:[1,0]
	v_pk_add_f32 v[178:179], v[178:179], s[16:17] op_sel_hi:[1,0]
	v_pk_mul_f32 v[126:127], v[126:127], v[222:223] op_sel:[0,1] op_sel_hi:[1,1]
	v_pk_mul_f32 v[128:129], v[128:129], v[222:223] op_sel:[0,1] op_sel_hi:[1,1]
	v_pk_mul_f32 v[118:119], v[118:119], v[222:223] op_sel:[0,1] op_sel_hi:[1,1]
	v_pk_mul_f32 v[120:121], v[120:121], v[222:223] op_sel:[0,1] op_sel_hi:[1,1]
	v_rcp_f32_e32 v172, v172
	v_rcp_f32_e32 v173, v173
	v_rcp_f32_e32 v174, v174
	v_rcp_f32_e32 v175, v175
	v_rcp_f32_e32 v176, v176
	v_rcp_f32_e32 v177, v177
	v_rcp_f32_e32 v178, v178
	v_rcp_f32_e32 v179, v179
	v_mov_b32_e32 v141, v140
	v_pk_mul_f32 v[126:127], v[126:127], v[172:173]
	v_pk_mul_f32 v[128:129], v[128:129], v[174:175]
	v_pk_mul_f32 v[118:119], v[118:119], v[176:177]
	v_pk_mul_f32 v[120:121], v[120:121], v[178:179]
	v_med3_f32 v126, v126, s70, v164
	v_med3_f32 v127, v127, s70, v164
	v_med3_f32 v128, v128, s70, v164
	v_med3_f32 v129, v129, s70, v164
	v_med3_f32 v118, v118, s70, v164
	v_med3_f32 v119, v119, s70, v164
	v_med3_f32 v120, v120, s70, v164
	v_med3_f32 v121, v121, s70, v164
	v_cvt_pk_fp8_f32 v180, v126, v127
	v_cvt_pk_fp8_f32 v181, v118, v119
	v_cvt_pk_fp8_f32 v180, v128, v129 op_sel:[0,0,1]
	v_cvt_pk_fp8_f32 v181, v120, v121 op_sel:[0,0,1]
	s_nop 1
	global_store_dwordx2 v141, v[180:181], s[6:7]
	v_cvt_f32_i32_e32 v108, v108
	v_cvt_f32_i32_e32 v109, v109
	v_cvt_f32_i32_e32 v110, v110
	v_cvt_f32_i32_e32 v111, v111
	v_cvt_f32_i32_e32 v100, v100
	v_cvt_f32_i32_e32 v101, v101
	v_cvt_f32_i32_e32 v102, v102
	v_cvt_f32_i32_e32 v103, v103
	v_cvt_f32_i32_e32 v104, v104
	v_cvt_f32_i32_e32 v105, v105
	v_cvt_f32_i32_e32 v106, v106
	v_cvt_f32_i32_e32 v107, v107
	v_cvt_f32_i32_e32 v96, v96
	v_cvt_f32_i32_e32 v97, v97
	v_cvt_f32_i32_e32 v98, v98
	v_cvt_f32_i32_e32 v99, v99
	v_pk_mul_f32 v[108:109], v[108:109], v[206:207]
	v_pk_mul_f32 v[110:111], v[110:111], v[208:209]
	v_pk_mul_f32 v[100:101], v[100:101], v[210:211]
	v_pk_mul_f32 v[102:103], v[102:103], v[212:213]
	v_pk_mul_f32 v[172:173], v[108:109], v[224:225] op_sel_hi:[1,0]
	v_pk_mul_f32 v[174:175], v[110:111], v[224:225] op_sel_hi:[1,0]
	v_pk_mul_f32 v[176:177], v[100:101], v[224:225] op_sel_hi:[1,0]
	v_pk_mul_f32 v[178:179], v[102:103], v[224:225] op_sel_hi:[1,0]
	v_pk_mul_f32 v[104:105], v[104:105], v[214:215]
	v_pk_mul_f32 v[106:107], v[106:107], v[216:217]
	v_pk_mul_f32 v[96:97], v[96:97], v[218:219]
	v_pk_mul_f32 v[98:99], v[98:99], v[220:221]
	v_exp_f32_e32 v172, v172
; __device__ __forceinline__ float sigmoidf_fast(float x) { return fast_rcp(1.0f + fast_exp2(-x * LOG2E)); }
; #define ROW_FENCE() asm volatile("" ::: "memory")
;     __device__ __forceinline__ void operator()(const pg8::i32x4 (&acc)[2][2][4][2], const pg8::Unit& u, int wr, int wc, int fr, int fq) const {
;     ...
;         for (int ai = 0; ai < 2; ++ai)
; #pragma unroll
;             for (int m = 0; m < 4; ++m) {
;                 const int row = u.pm * 256 + ai * 128 + wr * 64 + m * 16 + fr; const float r = rsv[ai][m];
;                 f32x4 h[2];
; #pragma unroll
;                 for (int n = 0; n < 2; ++n)
; #pragma unroll
;                     for (int j = 0; j < 4; ++j) { const float a1 = (float)acc[ai][0][m][n][j] * (r * c1[n][j]), a3 = (float)acc[ai][1][m][n][j] * (r * c3[n][j]); h[n][j] = a1 * sigmoidf_fast(a1) * a3; }
;                 u32x2 w;
; #pragma unroll
;                 for (int n = 0; n < 2; ++n) { int pk = __builtin_amdgcn_cvt_pk_fp8_f32(__builtin_amdgcn_fmed3f(h[n][0], -448.f, 448.f), __builtin_amdgcn_fmed3f(h[n][1], -448.f, 448.f), 0, false);
;                     pk = __builtin_amdgcn_cvt_pk_fp8_f32(__builtin_amdgcn_fmed3f(h[n][2], -448.f, 448.f), __builtin_amdgcn_fmed3f(h[n][3], -448.f, 448.f), pk, true); w[n] = (unsigned)pk; }
;                 if (!dry) *(u32x2*)(H + (size_t)(row - roff) * DFF + u.pn * 128 + wc * 32 + 8 * fq) = w;
;                 ROW_FENCE();
	v_exp_f32_e32 v173, v173
	v_exp_f32_e32 v174, v174
	v_exp_f32_e32 v175, v175
	v_exp_f32_e32 v176, v176
	v_exp_f32_e32 v177, v177
	v_exp_f32_e32 v178, v178
	v_exp_f32_e32 v179, v179
	v_pk_mul_f32 v[108:109], v[108:109], v[104:105]
	v_pk_mul_f32 v[110:111], v[110:111], v[106:107]
	v_pk_mul_f32 v[100:101], v[100:101], v[96:97]
	v_pk_mul_f32 v[102:103], v[102:103], v[98:99]
	v_pk_add_f32 v[172:173], v[172:173], s[16:17] op_sel_hi:[1,0]
	v_pk_add_f32 v[174:175], v[174:175], s[16:17] op_sel_hi:[1,0]
	v_pk_add_f32 v[176:177], v[176:177], s[16:17] op_sel_hi:[1,0]
	v_pk_add_f32 v[178:179], v[178:179], s[16:17] op_sel_hi:[1,0]
	v_pk_mul_f32 v[108:109], v[108:109], v[224:225] op_sel:[0,1] op_sel_hi:[1,1]
	v_pk_mul_f32 v[110:111], v[110:111], v[224:225] op_sel:[0,1] op_sel_hi:[1,1]
	v_pk_mul_f32 v[100:101], v[100:101], v[224:225] op_sel:[0,1] op_sel_hi:[1,1]
	v_pk_mul_f32 v[102:103], v[102:103], v[224:225] op_sel:[0,1] op_sel_hi:[1,1]
	v_rcp_f32_e32 v172, v172
	v_rcp_f32_e32 v173, v173
	v_rcp_f32_e32 v174, v174
	v_rcp_f32_e32 v175, v175
	v_rcp_f32_e32 v176, v176
	v_rcp_f32_e32 v177, v177
	v_rcp_f32_e32 v178, v178
	v_rcp_f32_e32 v179, v179
	v_add_u32_e32 v141, 0xe000, v140
	v_pk_mul_f32 v[108:109], v[108:109], v[172:173]
	v_pk_mul_f32 v[110:111], v[110:111], v[174:175]
	v_pk_mul_f32 v[100:101], v[100:101], v[176:177]
	v_pk_mul_f32 v[102:103], v[102:103], v[178:179]
	v_med3_f32 v108, v108, s70, v164
	v_med3_f32 v109, v109, s70, v164
	v_med3_f32 v110, v110, s70, v164
	v_med3_f32 v111, v111, s70, v164
	v_med3_f32 v100, v100, s70, v164
	v_med3_f32 v101, v101, s70, v164
	v_med3_f32 v102, v102, s70, v164
	v_med3_f32 v103, v103, s70, v164
	v_cvt_pk_fp8_f32 v182, v108, v109
	v_cvt_pk_fp8_f32 v183, v100, v101
	v_cvt_pk_fp8_f32 v182, v110, v111 op_sel:[0,0,1]
	v_cvt_pk_fp8_f32 v183, v102, v103 op_sel:[0,0,1]
	s_nop 1
	global_store_dwordx2 v141, v[182:183], s[6:7]
	v_cvt_f32_i32_e32 v92, v92
	v_cvt_f32_i32_e32 v93, v93
	v_cvt_f32_i32_e32 v94, v94
	v_cvt_f32_i32_e32 v95, v95
	v_cvt_f32_i32_e32 v84, v84
	v_cvt_f32_i32_e32 v85, v85
	v_cvt_f32_i32_e32 v86, v86
	v_cvt_f32_i32_e32 v87, v87
	v_cvt_f32_i32_e32 v88, v88
	v_cvt_f32_i32_e32 v89, v89
	v_cvt_f32_i32_e32 v90, v90
	v_cvt_f32_i32_e32 v91, v91
	v_cvt_f32_i32_e32 v80, v80
	v_cvt_f32_i32_e32 v81, v81
	v_cvt_f32_i32_e32 v82, v82
	v_cvt_f32_i32_e32 v83, v83
	v_pk_mul_f32 v[92:93], v[92:93], v[206:207]
	v_pk_mul_f32 v[94:95], v[94:95], v[208:209]
	v_pk_mul_f32 v[84:85], v[84:85], v[210:211]
	v_pk_mul_f32 v[86:87], v[86:87], v[212:213]
	v_pk_mul_f32 v[172:173], v[92:93], v[226:227] op_sel_hi:[1,0]
	v_pk_mul_f32 v[174:175], v[94:95], v[226:227] op_sel_hi:[1,0]
	v_pk_mul_f32 v[176:177], v[84:85], v[226:227] op_sel_hi:[1,0]
	v_pk_mul_f32 v[178:179], v[86:87], v[226:227] op_sel_hi:[1,0]
	v_pk_mul_f32 v[88:89], v[88:89], v[214:215]
	v_pk_mul_f32 v[90:91], v[90:91], v[216:217]
	v_pk_mul_f32 v[80:81], v[80:81], v[218:219]
	v_pk_mul_f32 v[82:83], v[82:83], v[220:221]
	v_exp_f32_e32 v172, v172
	v_exp_f32_e32 v173, v173
	v_exp_f32_e32 v174, v174
	v_exp_f32_e32 v175, v175
	v_exp_f32_e32 v176, v176
	v_exp_f32_e32 v177, v177
	v_exp_f32_e32 v178, v178
	v_exp_f32_e32 v179, v179
	v_pk_mul_f32 v[92:93], v[92:93], v[88:89]
	v_pk_mul_f32 v[94:95], v[94:95], v[90:91]
	v_pk_mul_f32 v[84:85], v[84:85], v[80:81]
	v_pk_mul_f32 v[86:87], v[86:87], v[82:83]
	v_pk_add_f32 v[172:173], v[172:173], s[16:17] op_sel_hi:[1,0]
	v_pk_add_f32 v[174:175], v[174:175], s[16:17] op_sel_hi:[1,0]
	v_pk_add_f32 v[176:177], v[176:177], s[16:17] op_sel_hi:[1,0]
	v_pk_add_f32 v[178:179], v[178:179], s[16:17] op_sel_hi:[1,0]
	v_pk_mul_f32 v[92:93], v[92:93], v[226:227] op_sel:[0,1] op_sel_hi:[1,1]
	v_pk_mul_f32 v[94:95], v[94:95], v[226:227] op_sel:[0,1] op_sel_hi:[1,1]
	v_pk_mul_f32 v[84:85], v[84:85], v[226:227] op_sel:[0,1] op_sel_hi:[1,1]
	v_pk_mul_f32 v[86:87], v[86:87], v[226:227] op_sel:[0,1] op_sel_hi:[1,1]
	v_rcp_f32_e32 v172, v172
	v_rcp_f32_e32 v173, v173
	v_rcp_f32_e32 v174, v174
	v_rcp_f32_e32 v175, v175
	v_rcp_f32_e32 v176, v176
	v_rcp_f32_e32 v177, v177
	v_rcp_f32_e32 v178, v178
	v_rcp_f32_e32 v179, v179
	v_add_u32_e32 v141, 0x1c000, v140
	v_pk_mul_f32 v[92:93], v[92:93], v[172:173]
	v_pk_mul_f32 v[94:95], v[94:95], v[174:175]
	v_pk_mul_f32 v[84:85], v[84:85], v[176:177]
	v_pk_mul_f32 v[86:87], v[86:87], v[178:179]
	v_med3_f32 v92, v92, s70, v164
	v_med3_f32 v93, v93, s70, v164
	v_med3_f32 v94, v94, s70, v164
	v_med3_f32 v95, v95, s70, v164
	v_med3_f32 v84, v84, s70, v164
	v_med3_f32 v85, v85, s70, v164
	v_med3_f32 v86, v86, s70, v164
	v_med3_f32 v87, v87, s70, v164
	v_cvt_pk_fp8_f32 v180, v92, v93
	v_cvt_pk_fp8_f32 v181, v84, v85
	v_cvt_pk_fp8_f32 v180, v94, v95 op_sel:[0,0,1]
	v_cvt_pk_fp8_f32 v181, v86, v87 op_sel:[0,0,1]
	s_nop 1
	global_store_dwordx2 v141, v[180:181], s[6:7]
	v_cvt_f32_i32_e32 v76, v76
	v_cvt_f32_i32_e32 v77, v77
	v_cvt_f32_i32_e32 v78, v78
	v_cvt_f32_i32_e32 v79, v79
	v_cvt_f32_i32_e32 v68, v68
	v_cvt_f32_i32_e32 v69, v69
	v_cvt_f32_i32_e32 v70, v70
	v_cvt_f32_i32_e32 v71, v71
	v_cvt_f32_i32_e32 v72, v72
	v_cvt_f32_i32_e32 v73, v73
	v_cvt_f32_i32_e32 v74, v74
	v_cvt_f32_i32_e32 v75, v75
	v_cvt_f32_i32_e32 v64, v64
	v_cvt_f32_i32_e32 v65, v65
	v_cvt_f32_i32_e32 v66, v66
	v_cvt_f32_i32_e32 v67, v67
	v_pk_mul_f32 v[76:77], v[76:77], v[206:207]
	v_pk_mul_f32 v[78:79], v[78:79], v[208:209]
	v_pk_mul_f32 v[68:69], v[68:69], v[210:211]
	v_pk_mul_f32 v[70:71], v[70:71], v[212:213]
	v_pk_mul_f32 v[172:173], v[76:77], v[228:229] op_sel_hi:[1,0]
	v_pk_mul_f32 v[174:175], v[78:79], v[228:229] op_sel_hi:[1,0]
	v_pk_mul_f32 v[176:177], v[68:69], v[228:229] op_sel_hi:[1,0]
	v_pk_mul_f32 v[178:179], v[70:71], v[228:229] op_sel_hi:[1,0]
; __device__ __forceinline__ float sigmoidf_fast(float x) { return fast_rcp(1.0f + fast_exp2(-x * LOG2E)); }
; #define ROW_FENCE() asm volatile("" ::: "memory")
;     __device__ __forceinline__ void operator()(const pg8::i32x4 (&acc)[2][2][4][2], const pg8::Unit& u, int wr, int wc, int fr, int fq) const {
;     ...
;         for (int ai = 0; ai < 2; ++ai)
; #pragma unroll
;             for (int m = 0; m < 4; ++m) {
;                 const int row = u.pm * 256 + ai * 128 + wr * 64 + m * 16 + fr; const float r = rsv[ai][m];
;                 f32x4 h[2];
; #pragma unroll
;                 for (int n = 0; n < 2; ++n)
; #pragma unroll
;                     for (int j = 0; j < 4; ++j) { const float a1 = (float)acc[ai][0][m][n][j] * (r * c1[n][j]), a3 = (float)acc[ai][1][m][n][j] * (r * c3[n][j]); h[n][j] = a1 * sigmoidf_fast(a1) * a3; }
;                 u32x2 w;
; #pragma unroll
;                 for (int n = 0; n < 2; ++n) { int pk = __builtin_amdgcn_cvt_pk_fp8_f32(__builtin_amdgcn_fmed3f(h[n][0], -448.f, 448.f), __builtin_amdgcn_fmed3f(h[n][1], -448.f, 448.f), 0, false);
;                     pk = __builtin_amdgcn_cvt_pk_fp8_f32(__builtin_amdgcn_fmed3f(h[n][2], -448.f, 448.f), __builtin_amdgcn_fmed3f(h[n][3], -448.f, 448.f), pk, true); w[n] = (unsigned)pk; }
;                 if (!dry) *(u32x2*)(H + (size_t)(row - roff) * DFF + u.pn * 128 + wc * 32 + 8 * fq) = w;
;                 ROW_FENCE();
;             }
	v_pk_mul_f32 v[72:73], v[72:73], v[214:215]
	v_pk_mul_f32 v[74:75], v[74:75], v[216:217]
	v_pk_mul_f32 v[64:65], v[64:65], v[218:219]
	v_pk_mul_f32 v[66:67], v[66:67], v[220:221]
	v_exp_f32_e32 v172, v172
	v_exp_f32_e32 v173, v173
	v_exp_f32_e32 v174, v174
	v_exp_f32_e32 v175, v175
	v_exp_f32_e32 v176, v176
	v_exp_f32_e32 v177, v177
	v_exp_f32_e32 v178, v178
	v_exp_f32_e32 v179, v179
	v_pk_mul_f32 v[76:77], v[76:77], v[72:73]
	v_pk_mul_f32 v[78:79], v[78:79], v[74:75]
	v_pk_mul_f32 v[68:69], v[68:69], v[64:65]
	v_pk_mul_f32 v[70:71], v[70:71], v[66:67]
	v_pk_add_f32 v[172:173], v[172:173], s[16:17] op_sel_hi:[1,0]
	v_pk_add_f32 v[174:175], v[174:175], s[16:17] op_sel_hi:[1,0]
	v_pk_add_f32 v[176:177], v[176:177], s[16:17] op_sel_hi:[1,0]
	v_pk_add_f32 v[178:179], v[178:179], s[16:17] op_sel_hi:[1,0]
	v_pk_mul_f32 v[76:77], v[76:77], v[228:229] op_sel:[0,1] op_sel_hi:[1,1]
	v_pk_mul_f32 v[78:79], v[78:79], v[228:229] op_sel:[0,1] op_sel_hi:[1,1]
	v_pk_mul_f32 v[68:69], v[68:69], v[228:229] op_sel:[0,1] op_sel_hi:[1,1]
	v_pk_mul_f32 v[70:71], v[70:71], v[228:229] op_sel:[0,1] op_sel_hi:[1,1]
	v_rcp_f32_e32 v172, v172
	v_rcp_f32_e32 v173, v173
	v_rcp_f32_e32 v174, v174
	v_rcp_f32_e32 v175, v175
	v_rcp_f32_e32 v176, v176
	v_rcp_f32_e32 v177, v177
	v_rcp_f32_e32 v178, v178
	v_rcp_f32_e32 v179, v179
	v_add_u32_e32 v141, 0x2a000, v140
	v_pk_mul_f32 v[76:77], v[76:77], v[172:173]
	v_pk_mul_f32 v[78:79], v[78:79], v[174:175]
	v_pk_mul_f32 v[68:69], v[68:69], v[176:177]
	v_pk_mul_f32 v[70:71], v[70:71], v[178:179]
	v_med3_f32 v76, v76, s70, v164
	v_med3_f32 v77, v77, s70, v164
	v_med3_f32 v78, v78, s70, v164
	v_med3_f32 v79, v79, s70, v164
	v_med3_f32 v68, v68, s70, v164
	v_med3_f32 v69, v69, s70, v164
	v_med3_f32 v70, v70, s70, v164
	v_med3_f32 v71, v71, s70, v164
	v_cvt_pk_fp8_f32 v182, v76, v77
	v_cvt_pk_fp8_f32 v183, v68, v69
	v_cvt_pk_fp8_f32 v182, v78, v79 op_sel:[0,0,1]
	v_cvt_pk_fp8_f32 v183, v70, v71 op_sel:[0,0,1]
	s_nop 1
	global_store_dwordx2 v141, v[182:183], s[6:7]
	v_cvt_f32_i32_e32 v60, v60
	v_cvt_f32_i32_e32 v61, v61
	v_cvt_f32_i32_e32 v62, v62
	v_cvt_f32_i32_e32 v63, v63
	v_cvt_f32_i32_e32 v52, v52
	v_cvt_f32_i32_e32 v53, v53
	v_cvt_f32_i32_e32 v54, v54
	v_cvt_f32_i32_e32 v55, v55
	v_cvt_f32_i32_e32 v56, v56
	v_cvt_f32_i32_e32 v57, v57
	v_cvt_f32_i32_e32 v58, v58
	v_cvt_f32_i32_e32 v59, v59
	v_cvt_f32_i32_e32 v48, v48
	v_cvt_f32_i32_e32 v49, v49
	v_cvt_f32_i32_e32 v50, v50
	v_cvt_f32_i32_e32 v51, v51
	v_pk_mul_f32 v[60:61], v[60:61], v[206:207]
	v_pk_mul_f32 v[62:63], v[62:63], v[208:209]
	v_pk_mul_f32 v[52:53], v[52:53], v[210:211]
	v_pk_mul_f32 v[54:55], v[54:55], v[212:213]
	v_pk_mul_f32 v[172:173], v[60:61], v[230:231] op_sel_hi:[1,0]
	v_pk_mul_f32 v[174:175], v[62:63], v[230:231] op_sel_hi:[1,0]
	v_pk_mul_f32 v[176:177], v[52:53], v[230:231] op_sel_hi:[1,0]
	v_pk_mul_f32 v[178:179], v[54:55], v[230:231] op_sel_hi:[1,0]
	v_pk_mul_f32 v[56:57], v[56:57], v[214:215]
	v_pk_mul_f32 v[58:59], v[58:59], v[216:217]
	v_pk_mul_f32 v[48:49], v[48:49], v[218:219]
	v_pk_mul_f32 v[50:51], v[50:51], v[220:221]
	v_exp_f32_e32 v172, v172
	v_exp_f32_e32 v173, v173
	v_exp_f32_e32 v174, v174
	v_exp_f32_e32 v175, v175
	v_exp_f32_e32 v176, v176
	v_exp_f32_e32 v177, v177
	v_exp_f32_e32 v178, v178
	v_exp_f32_e32 v179, v179
	v_pk_mul_f32 v[60:61], v[60:61], v[56:57]
	v_pk_mul_f32 v[62:63], v[62:63], v[58:59]
	v_pk_mul_f32 v[52:53], v[52:53], v[48:49]
	v_pk_mul_f32 v[54:55], v[54:55], v[50:51]
	v_pk_add_f32 v[172:173], v[172:173], s[16:17] op_sel_hi:[1,0]
	v_pk_add_f32 v[174:175], v[174:175], s[16:17] op_sel_hi:[1,0]
	v_pk_add_f32 v[176:177], v[176:177], s[16:17] op_sel_hi:[1,0]
	v_pk_add_f32 v[178:179], v[178:179], s[16:17] op_sel_hi:[1,0]
	v_pk_mul_f32 v[60:61], v[60:61], v[230:231] op_sel:[0,1] op_sel_hi:[1,1]
	v_pk_mul_f32 v[62:63], v[62:63], v[230:231] op_sel:[0,1] op_sel_hi:[1,1]
	v_pk_mul_f32 v[52:53], v[52:53], v[230:231] op_sel:[0,1] op_sel_hi:[1,1]
	v_pk_mul_f32 v[54:55], v[54:55], v[230:231] op_sel:[0,1] op_sel_hi:[1,1]
	v_rcp_f32_e32 v172, v172
	v_rcp_f32_e32 v173, v173
	v_rcp_f32_e32 v174, v174
	v_rcp_f32_e32 v175, v175
	v_rcp_f32_e32 v176, v176
	v_rcp_f32_e32 v177, v177
	v_rcp_f32_e32 v178, v178
	v_rcp_f32_e32 v179, v179
	v_add_u32_e32 v141, 0x70000, v140
	v_pk_mul_f32 v[60:61], v[60:61], v[172:173]
	v_pk_mul_f32 v[62:63], v[62:63], v[174:175]
	v_pk_mul_f32 v[52:53], v[52:53], v[176:177]
	v_pk_mul_f32 v[54:55], v[54:55], v[178:179]
	v_med3_f32 v60, v60, s70, v164
	v_med3_f32 v61, v61, s70, v164
	v_med3_f32 v62, v62, s70, v164
	v_med3_f32 v63, v63, s70, v164
	v_med3_f32 v52, v52, s70, v164
	v_med3_f32 v53, v53, s70, v164
	v_med3_f32 v54, v54, s70, v164
	v_med3_f32 v55, v55, s70, v164
	v_cvt_pk_fp8_f32 v180, v60, v61
	v_cvt_pk_fp8_f32 v181, v52, v53
	v_cvt_pk_fp8_f32 v180, v62, v63 op_sel:[0,0,1]
	v_cvt_pk_fp8_f32 v181, v54, v55 op_sel:[0,0,1]
	s_nop 1
	global_store_dwordx2 v141, v[180:181], s[6:7]
	v_cvt_f32_i32_e32 v44, v44
	v_cvt_f32_i32_e32 v45, v45
	v_cvt_f32_i32_e32 v46, v46
	v_cvt_f32_i32_e32 v47, v47
	v_cvt_f32_i32_e32 v36, v36
	v_cvt_f32_i32_e32 v37, v37
	v_cvt_f32_i32_e32 v38, v38
	v_cvt_f32_i32_e32 v39, v39
	v_cvt_f32_i32_e32 v40, v40
	v_cvt_f32_i32_e32 v41, v41
	v_cvt_f32_i32_e32 v42, v42
	v_cvt_f32_i32_e32 v43, v43
	v_cvt_f32_i32_e32 v32, v32
	v_cvt_f32_i32_e32 v33, v33
	v_cvt_f32_i32_e32 v34, v34
	v_cvt_f32_i32_e32 v35, v35
	v_pk_mul_f32 v[44:45], v[44:45], v[206:207]
	v_pk_mul_f32 v[46:47], v[46:47], v[208:209]
	v_pk_mul_f32 v[36:37], v[36:37], v[210:211]
	v_pk_mul_f32 v[38:39], v[38:39], v[212:213]
	v_pk_mul_f32 v[172:173], v[44:45], v[232:233] op_sel_hi:[1,0]
	v_pk_mul_f32 v[174:175], v[46:47], v[232:233] op_sel_hi:[1,0]
; __device__ __forceinline__ float sigmoidf_fast(float x) { return fast_rcp(1.0f + fast_exp2(-x * LOG2E)); }
; #define ROW_FENCE() asm volatile("" ::: "memory")
;     __device__ __forceinline__ void operator()(const pg8::i32x4 (&acc)[2][2][4][2], const pg8::Unit& u, int wr, int wc, int fr, int fq) const {
;     ...
;         for (int ai = 0; ai < 2; ++ai)
; #pragma unroll
;             for (int m = 0; m < 4; ++m) {
;                 const int row = u.pm * 256 + ai * 128 + wr * 64 + m * 16 + fr; const float r = rsv[ai][m];
;                 f32x4 h[2];
; #pragma unroll
;                 for (int n = 0; n < 2; ++n)
; #pragma unroll
;                     for (int j = 0; j < 4; ++j) { const float a1 = (float)acc[ai][0][m][n][j] * (r * c1[n][j]), a3 = (float)acc[ai][1][m][n][j] * (r * c3[n][j]); h[n][j] = a1 * sigmoidf_fast(a1) * a3; }
;                 u32x2 w;
; #pragma unroll
;                 for (int n = 0; n < 2; ++n) { int pk = __builtin_amdgcn_cvt_pk_fp8_f32(__builtin_amdgcn_fmed3f(h[n][0], -448.f, 448.f), __builtin_amdgcn_fmed3f(h[n][1], -448.f, 448.f), 0, false);
;                     pk = __builtin_amdgcn_cvt_pk_fp8_f32(__builtin_amdgcn_fmed3f(h[n][2], -448.f, 448.f), __builtin_amdgcn_fmed3f(h[n][3], -448.f, 448.f), pk, true); w[n] = (unsigned)pk; }
;                 if (!dry) *(u32x2*)(H + (size_t)(row - roff) * DFF + u.pn * 128 + wc * 32 + 8 * fq) = w;
;                 ROW_FENCE();
;             }
	v_pk_mul_f32 v[176:177], v[36:37], v[232:233] op_sel_hi:[1,0]
	v_pk_mul_f32 v[178:179], v[38:39], v[232:233] op_sel_hi:[1,0]
	v_pk_mul_f32 v[40:41], v[40:41], v[214:215]
	v_pk_mul_f32 v[42:43], v[42:43], v[216:217]
	v_pk_mul_f32 v[32:33], v[32:33], v[218:219]
	v_pk_mul_f32 v[34:35], v[34:35], v[220:221]
	v_exp_f32_e32 v172, v172
	v_exp_f32_e32 v173, v173
	v_exp_f32_e32 v174, v174
	v_exp_f32_e32 v175, v175
	v_exp_f32_e32 v176, v176
	v_exp_f32_e32 v177, v177
	v_exp_f32_e32 v178, v178
	v_exp_f32_e32 v179, v179
	v_pk_mul_f32 v[44:45], v[44:45], v[40:41]
	v_pk_mul_f32 v[46:47], v[46:47], v[42:43]
	v_pk_mul_f32 v[36:37], v[36:37], v[32:33]
	v_pk_mul_f32 v[38:39], v[38:39], v[34:35]
	v_pk_add_f32 v[172:173], v[172:173], s[16:17] op_sel_hi:[1,0]
	v_pk_add_f32 v[174:175], v[174:175], s[16:17] op_sel_hi:[1,0]
	v_pk_add_f32 v[176:177], v[176:177], s[16:17] op_sel_hi:[1,0]
	v_pk_add_f32 v[178:179], v[178:179], s[16:17] op_sel_hi:[1,0]
	v_pk_mul_f32 v[44:45], v[44:45], v[232:233] op_sel:[0,1] op_sel_hi:[1,1]
	v_pk_mul_f32 v[46:47], v[46:47], v[232:233] op_sel:[0,1] op_sel_hi:[1,1]
	v_pk_mul_f32 v[36:37], v[36:37], v[232:233] op_sel:[0,1] op_sel_hi:[1,1]
	v_pk_mul_f32 v[38:39], v[38:39], v[232:233] op_sel:[0,1] op_sel_hi:[1,1]
	v_rcp_f32_e32 v172, v172
	v_rcp_f32_e32 v173, v173
	v_rcp_f32_e32 v174, v174
	v_rcp_f32_e32 v175, v175
	v_rcp_f32_e32 v176, v176
	v_rcp_f32_e32 v177, v177
	v_rcp_f32_e32 v178, v178
	v_rcp_f32_e32 v179, v179
	v_add_u32_e32 v141, 0x7e000, v140
	v_pk_mul_f32 v[44:45], v[44:45], v[172:173]
	v_pk_mul_f32 v[46:47], v[46:47], v[174:175]
	v_pk_mul_f32 v[36:37], v[36:37], v[176:177]
	v_pk_mul_f32 v[38:39], v[38:39], v[178:179]
	v_med3_f32 v44, v44, s70, v164
	v_med3_f32 v45, v45, s70, v164
	v_med3_f32 v46, v46, s70, v164
	v_med3_f32 v47, v47, s70, v164
	v_med3_f32 v36, v36, s70, v164
	v_med3_f32 v37, v37, s70, v164
	v_med3_f32 v38, v38, s70, v164
	v_med3_f32 v39, v39, s70, v164
	v_cvt_pk_fp8_f32 v182, v44, v45
	v_cvt_pk_fp8_f32 v183, v36, v37
	v_cvt_pk_fp8_f32 v182, v46, v47 op_sel:[0,0,1]
	v_cvt_pk_fp8_f32 v183, v38, v39 op_sel:[0,0,1]
	s_nop 1
	global_store_dwordx2 v141, v[182:183], s[6:7]
	v_cvt_f32_i32_e32 v28, v28
	v_cvt_f32_i32_e32 v29, v29
	v_cvt_f32_i32_e32 v30, v30
	v_cvt_f32_i32_e32 v31, v31
	v_cvt_f32_i32_e32 v20, v20
	v_cvt_f32_i32_e32 v21, v21
	v_cvt_f32_i32_e32 v22, v22
	v_cvt_f32_i32_e32 v23, v23
	v_cvt_f32_i32_e32 v24, v24
	v_cvt_f32_i32_e32 v25, v25
	v_cvt_f32_i32_e32 v26, v26
	v_cvt_f32_i32_e32 v27, v27
	v_cvt_f32_i32_e32 v16, v16
	v_cvt_f32_i32_e32 v17, v17
	v_cvt_f32_i32_e32 v18, v18
	v_cvt_f32_i32_e32 v19, v19
	v_pk_mul_f32 v[28:29], v[28:29], v[206:207]
	v_pk_mul_f32 v[30:31], v[30:31], v[208:209]
	v_pk_mul_f32 v[20:21], v[20:21], v[210:211]
	v_pk_mul_f32 v[22:23], v[22:23], v[212:213]
	v_pk_mul_f32 v[172:173], v[28:29], v[234:235] op_sel_hi:[1,0]
	v_pk_mul_f32 v[174:175], v[30:31], v[234:235] op_sel_hi:[1,0]
	v_pk_mul_f32 v[176:177], v[20:21], v[234:235] op_sel_hi:[1,0]
	v_pk_mul_f32 v[178:179], v[22:23], v[234:235] op_sel_hi:[1,0]
	v_pk_mul_f32 v[24:25], v[24:25], v[214:215]
	v_pk_mul_f32 v[26:27], v[26:27], v[216:217]
	v_pk_mul_f32 v[16:17], v[16:17], v[218:219]
	v_pk_mul_f32 v[18:19], v[18:19], v[220:221]
	v_exp_f32_e32 v172, v172
	v_exp_f32_e32 v173, v173
	v_exp_f32_e32 v174, v174
	v_exp_f32_e32 v175, v175
	v_exp_f32_e32 v176, v176
	v_exp_f32_e32 v177, v177
	v_exp_f32_e32 v178, v178
	v_exp_f32_e32 v179, v179
	v_pk_mul_f32 v[28:29], v[28:29], v[24:25]
	v_pk_mul_f32 v[30:31], v[30:31], v[26:27]
	v_pk_mul_f32 v[20:21], v[20:21], v[16:17]
	v_pk_mul_f32 v[22:23], v[22:23], v[18:19]
	v_pk_add_f32 v[172:173], v[172:173], s[16:17] op_sel_hi:[1,0]
	v_pk_add_f32 v[174:175], v[174:175], s[16:17] op_sel_hi:[1,0]
	v_pk_add_f32 v[176:177], v[176:177], s[16:17] op_sel_hi:[1,0]
	v_pk_add_f32 v[178:179], v[178:179], s[16:17] op_sel_hi:[1,0]
	v_pk_mul_f32 v[28:29], v[28:29], v[234:235] op_sel:[0,1] op_sel_hi:[1,1]
	v_pk_mul_f32 v[30:31], v[30:31], v[234:235] op_sel:[0,1] op_sel_hi:[1,1]
; __device__ __forceinline__ float sigmoidf_fast(float x) { return fast_rcp(1.0f + fast_exp2(-x * LOG2E)); }
; #define PG8_BAR __builtin_amdgcn_s_barrier()
; #define ROW_FENCE() asm volatile("" ::: "memory")
; template <class Epi, class Sched, bool ALIGN_EPI = true, bool SP2 = true, bool I8 = false, bool F8 = false>
; __device__ __forceinline__ void gemm_phase(LAS unsigned char* lds, const int K, const Sched& S, const Epi& E, const int wave) {
;     ...
;         if (!has_next) break;
;         if (!(Epi::KEEPS && cur.sub < 2)) {
; #pragma unroll
;         for (int a = 0; a < 2; ++a)
; #pragma unroll
;             for (int b = 0; b < 2; ++b)
; #pragma unroll
;                 for (int m = 0; m < 4; ++m)
; #pragma unroll
;                     for (int n = 0; n < 2; ++n) acc[a][b][m][n] = (acc_t){0, 0, 0, 0};
;         }
;         cur = nxt; cA = nA; cB = nB; ++ui;
;         if constexpr (ALIGN_EPI) { if (wr == 1) PG8_BAR; }
;     __device__ __forceinline__ void operator()(const pg8::i32x4 (&acc)[2][2][4][2], const pg8::Unit& u, int wr, int wc, int fr, int fq) const {
;     ...
;         for (int ai = 0; ai < 2; ++ai)
; #pragma unroll
;             for (int m = 0; m < 4; ++m) {
;                 const int row = u.pm * 256 + ai * 128 + wr * 64 + m * 16 + fr; const float r = rsv[ai][m];
;                 f32x4 h[2];
; #pragma unroll
;                 for (int n = 0; n < 2; ++n)
; #pragma unroll
;                     for (int j = 0; j < 4; ++j) { const float a1 = (float)acc[ai][0][m][n][j] * (r * c1[n][j]), a3 = (float)acc[ai][1][m][n][j] * (r * c3[n][j]); h[n][j] = a1 * sigmoidf_fast(a1) * a3; }
;                 u32x2 w;
; #pragma unroll
;                 for (int n = 0; n < 2; ++n) { int pk = __builtin_amdgcn_cvt_pk_fp8_f32(__builtin_amdgcn_fmed3f(h[n][0], -448.f, 448.f), __builtin_amdgcn_fmed3f(h[n][1], -448.f, 448.f), 0, false);
;                     pk = __builtin_amdgcn_cvt_pk_fp8_f32(__builtin_amdgcn_fmed3f(h[n][2], -448.f, 448.f), __builtin_amdgcn_fmed3f(h[n][3], -448.f, 448.f), pk, true); w[n] = (unsigned)pk; }
;                 if (!dry) *(u32x2*)(H + (size_t)(row - roff) * DFF + u.pn * 128 + wc * 32 + 8 * fq) = w;
;                 ROW_FENCE();
;             }
	v_pk_mul_f32 v[20:21], v[20:21], v[234:235] op_sel:[0,1] op_sel_hi:[1,1]
	v_pk_mul_f32 v[22:23], v[22:23], v[234:235] op_sel:[0,1] op_sel_hi:[1,1]
	v_rcp_f32_e32 v172, v172
	v_rcp_f32_e32 v173, v173
	v_rcp_f32_e32 v174, v174
	v_rcp_f32_e32 v175, v175
	v_rcp_f32_e32 v176, v176
	v_rcp_f32_e32 v177, v177
	v_rcp_f32_e32 v178, v178
	v_rcp_f32_e32 v179, v179
	v_add_u32_e32 v141, 0x8c000, v140
	v_pk_mul_f32 v[28:29], v[28:29], v[172:173]
	v_pk_mul_f32 v[30:31], v[30:31], v[174:175]
	v_pk_mul_f32 v[20:21], v[20:21], v[176:177]
	v_pk_mul_f32 v[22:23], v[22:23], v[178:179]
	v_med3_f32 v28, v28, s70, v164
	v_med3_f32 v29, v29, s70, v164
	v_med3_f32 v30, v30, s70, v164
	v_med3_f32 v31, v31, s70, v164
	v_med3_f32 v20, v20, s70, v164
	v_med3_f32 v21, v21, s70, v164
	v_med3_f32 v22, v22, s70, v164
	v_med3_f32 v23, v23, s70, v164
	v_cvt_pk_fp8_f32 v180, v28, v29
	v_cvt_pk_fp8_f32 v181, v20, v21
	v_cvt_pk_fp8_f32 v180, v30, v31 op_sel:[0,0,1]
	v_cvt_pk_fp8_f32 v181, v22, v23 op_sel:[0,0,1]
	s_nop 1
	global_store_dwordx2 v141, v[180:181], s[6:7]
	v_cvt_f32_i32_e32 v12, v12
	v_cvt_f32_i32_e32 v13, v13
	v_cvt_f32_i32_e32 v14, v14
	v_cvt_f32_i32_e32 v15, v15
	v_cvt_f32_i32_e32 v4, v4
	v_cvt_f32_i32_e32 v5, v5
	v_cvt_f32_i32_e32 v6, v6
	v_cvt_f32_i32_e32 v7, v7
	v_cvt_f32_i32_e32 v8, v8
	v_cvt_f32_i32_e32 v9, v9
	v_cvt_f32_i32_e32 v10, v10
	v_cvt_f32_i32_e32 v11, v11
	v_cvt_f32_i32_e32 v0, v0
	v_cvt_f32_i32_e32 v1, v1
	v_cvt_f32_i32_e32 v2, v2
	v_cvt_f32_i32_e32 v3, v3
	v_pk_mul_f32 v[12:13], v[12:13], v[206:207]
	v_pk_mul_f32 v[14:15], v[14:15], v[208:209]
	v_pk_mul_f32 v[4:5], v[4:5], v[210:211]
	v_pk_mul_f32 v[6:7], v[6:7], v[212:213]
	v_pk_mul_f32 v[172:173], v[12:13], v[236:237] op_sel_hi:[1,0]
	v_pk_mul_f32 v[174:175], v[14:15], v[236:237] op_sel_hi:[1,0]
	v_pk_mul_f32 v[176:177], v[4:5], v[236:237] op_sel_hi:[1,0]
	v_pk_mul_f32 v[178:179], v[6:7], v[236:237] op_sel_hi:[1,0]
	v_pk_mul_f32 v[8:9], v[8:9], v[214:215]
	v_pk_mul_f32 v[10:11], v[10:11], v[216:217]
	v_pk_mul_f32 v[0:1], v[0:1], v[218:219]
	v_pk_mul_f32 v[2:3], v[2:3], v[220:221]
	v_exp_f32_e32 v172, v172
	v_exp_f32_e32 v173, v173
	v_exp_f32_e32 v174, v174
	v_exp_f32_e32 v175, v175
	v_exp_f32_e32 v176, v176
	v_exp_f32_e32 v177, v177
	v_exp_f32_e32 v178, v178
	v_exp_f32_e32 v179, v179
	v_pk_mul_f32 v[12:13], v[12:13], v[8:9]
	v_pk_mul_f32 v[14:15], v[14:15], v[10:11]
	v_pk_mul_f32 v[4:5], v[4:5], v[0:1]
	v_pk_mul_f32 v[6:7], v[6:7], v[2:3]
	v_pk_add_f32 v[172:173], v[172:173], s[16:17] op_sel_hi:[1,0]
	v_pk_add_f32 v[174:175], v[174:175], s[16:17] op_sel_hi:[1,0]
	v_pk_add_f32 v[176:177], v[176:177], s[16:17] op_sel_hi:[1,0]
	v_pk_add_f32 v[178:179], v[178:179], s[16:17] op_sel_hi:[1,0]
	v_pk_mul_f32 v[12:13], v[12:13], v[236:237] op_sel:[0,1] op_sel_hi:[1,1]
	v_pk_mul_f32 v[14:15], v[14:15], v[236:237] op_sel:[0,1] op_sel_hi:[1,1]
	v_pk_mul_f32 v[4:5], v[4:5], v[236:237] op_sel:[0,1] op_sel_hi:[1,1]
	v_pk_mul_f32 v[6:7], v[6:7], v[236:237] op_sel:[0,1] op_sel_hi:[1,1]
	v_rcp_f32_e32 v172, v172
	v_rcp_f32_e32 v173, v173
	v_rcp_f32_e32 v174, v174
	v_rcp_f32_e32 v175, v175
	v_rcp_f32_e32 v176, v176
	v_rcp_f32_e32 v177, v177
	v_rcp_f32_e32 v178, v178
	v_rcp_f32_e32 v179, v179
	v_add_u32_e32 v141, 0x9a000, v140
	v_pk_mul_f32 v[12:13], v[12:13], v[172:173]
	v_pk_mul_f32 v[14:15], v[14:15], v[174:175]
	v_pk_mul_f32 v[4:5], v[4:5], v[176:177]
	v_pk_mul_f32 v[6:7], v[6:7], v[178:179]
	v_med3_f32 v12, v12, s70, v164
	v_med3_f32 v13, v13, s70, v164
	v_med3_f32 v14, v14, s70, v164
	v_med3_f32 v15, v15, s70, v164
	v_med3_f32 v4, v4, s70, v164
	v_med3_f32 v5, v5, s70, v164
	v_med3_f32 v6, v6, s70, v164
	v_med3_f32 v7, v7, s70, v164
	v_cvt_pk_fp8_f32 v182, v12, v13
	v_cvt_pk_fp8_f32 v183, v4, v5
	v_cvt_pk_fp8_f32 v182, v14, v15 op_sel:[0,0,1]
	v_cvt_pk_fp8_f32 v183, v6, v7 op_sel:[0,0,1]
	s_nop 1
	global_store_dwordx2 v141, v[182:183], s[6:7]
	s_andn2_b64 vcc, exec, s[0:1]
	s_mov_b64 s[16:17], -1
	s_cbranch_vccnz .LBB0_1763
	s_andn2_b64 vcc, exec, s[2:3]
	s_cbranch_vccnz .LBB0_1762
	s_barrier
	s_branch .LBB0_1762
